# barrier-side conversions: dedupe the duplicated single-item load/store batch, 7 side waves per barrier (was 3), P5 slot 33->13 items, P7 queue shortened; plus cache policies
# speedup vs baseline: 1.0345x; 1.0079x over previous
.LBB0_56:
	s_cmp_gt_i32 s95, 1
	s_cselect_b64 s[6:7], -1, 0
	s_and_b64 s[0:1], s[4:5], s[6:7]
	s_andn2_b64 vcc, exec, s[0:1]
	s_cbranch_vccnz .LBB0_134
	s_waitcnt vmcnt(0)
	v_readlane_b32 s0, v255, 0
	s_cmp_gt_u32 s0, 63
	s_mov_b64 s[4:5], -1
	s_barrier
	s_cbranch_scc0 .LBB0_79
	v_readlane_b32 s0, v255, 0
	s_cmpk_gt_u32 s0, 0x1ff
	s_cbranch_scc1 .LBB0_78
	v_readlane_b32 s0, v255, 4
	s_mul_i32 s1, s0, 7
	v_readlane_b32 s0, v255, 28
	s_add_i32 s1, s1, s0
	s_add_i32 s0, s1, 0xdcff
	s_cmp_gt_i32 s0, 0xffff
	s_cselect_b64 s[12:13], -1, 0
	s_and_b64 vcc, exec, s[12:13]
	s_waitcnt vmcnt(5)
	v_mbcnt_lo_u32_b32 v0, -1, 0
	v_mbcnt_hi_u32_b32 v0, -1, v0
	s_cbranch_vccz .LBB0_62
	s_cmp_lt_u32 s0, 0x18000
	s_cbranch_scc0 .LBB0_63
	s_add_i32 s2, s1, 0xffffdcff
	s_lshr_b32 s8, s2, 10
	s_mov_b32 s9, 0
	s_lshl_b64 s[2:3], s[8:9], 22
	s_lshl_b64 s[4:5], s[8:9], 24
	s_add_u32 s10, s70, s4
	s_addc_u32 s11, s71, s5
	s_add_u32 s2, s90, s2
	s_addc_u32 s3, s91, s3
	s_add_u32 s4, s2, 0x3b100000
	s_addc_u32 s5, s3, 0
	s_lshl_b32 s2, s0, 1
	s_and_b32 s8, s2, 0x780
	s_lshl_b32 s2, s8, 13
	s_add_u32 s2, s10, s2
	s_addc_u32 s3, s11, 0
	s_lshl_b32 s10, s0, 5
	s_and_b32 s10, s10, 0x7e0
	s_lshl_b32 s14, s10, 2
	s_add_u32 s14, s2, s14
	s_mov_b32 s11, s9
	s_addc_u32 s15, s3, 0
	s_mov_b64 s[16:17], 0
	s_branch .LBB0_64

.LBB0_68:
	v_lshlrev_b32_e32 v1, 1, v0
	v_and_b32_e32 v130, -16, v1
	v_lshlrev_b32_e32 v0, 2, v0
	v_and_b32_e32 v48, 28, v0
	v_mad_i64_i32 v[0:1], s[18:19], s16, v130, 0
	v_mov_b32_e32 v67, 0
	v_lshl_add_u64 v[0:1], v[0:1], 2, s[14:15]
	v_lshlrev_b32_e32 v66, 2, v48
	s_mov_b32 s3, 0
	v_lshl_add_u64 v[62:63], v[0:1], 0, v[66:67]
	s_mul_i32 s2, s16, 60
	v_lshl_add_u64 v[24:25], v[62:63], 0, s[2:3]
	s_lshl_b32 s2, s16, 2
	s_sub_u32 s2, 0, s2
	s_subb_u32 s3, 0, 0
	v_lshl_add_u64 v[0:1], v[24:25], 0, s[2:3]
	v_lshl_add_u64 v[8:9], v[0:1], 0, s[2:3]
	global_load_dwordx4 v[0:3], v[0:1], off sc1 nt
	s_nop 0
	global_load_dwordx4 v[4:7], v[8:9], off sc1 nt
	v_lshl_add_u64 v[8:9], v[8:9], 0, s[2:3]
	v_lshl_add_u64 v[16:17], v[8:9], 0, s[2:3]
	global_load_dwordx4 v[8:11], v[8:9], off sc1 nt
	s_nop 0
	global_load_dwordx4 v[12:15], v[16:17], off sc1 nt
	v_lshl_add_u64 v[16:17], v[16:17], 0, s[2:3]
	v_lshl_add_u64 v[26:27], v[16:17], 0, s[2:3]
	global_load_dwordx4 v[16:19], v[16:17], off sc1 nt
	s_nop 0
	global_load_dwordx4 v[20:23], v[26:27], off sc1 nt
	v_lshl_add_u64 v[26:27], v[26:27], 0, s[2:3]
	global_load_dwordx4 v[28:31], v[26:27], off sc1 nt
	v_lshl_add_u64 v[26:27], v[26:27], 0, s[2:3]
	global_load_dwordx4 v[32:35], v[26:27], off sc1 nt
	v_lshl_add_u64 v[26:27], v[26:27], 0, s[2:3]
	global_load_dwordx4 v[36:39], v[26:27], off sc1 nt
	v_lshl_add_u64 v[26:27], v[26:27], 0, s[2:3]
	global_load_dwordx4 v[40:43], v[26:27], off sc1 nt
	v_lshl_add_u64 v[26:27], v[26:27], 0, s[2:3]
	global_load_dwordx4 v[44:47], v[26:27], off sc1 nt
	v_lshl_add_u64 v[26:27], v[26:27], 0, s[2:3]
	global_load_dwordx4 v[50:53], v[26:27], off sc1 nt
	v_lshl_add_u64 v[26:27], v[26:27], 0, s[2:3]
	global_load_dwordx4 v[54:57], v[26:27], off sc1 nt
	v_lshl_add_u64 v[26:27], v[26:27], 0, s[2:3]
	global_load_dwordx4 v[58:61], v[26:27], off sc1 nt
	s_nop 0
	global_load_dwordx4 v[24:27], v[24:25], off sc1 nt
	s_nop 0
	global_load_dwordx4 v[62:65], v[62:63], off sc1 nt
	v_ashrrev_i32_e32 v131, 31, v130
	s_and_b64 vcc, exec, s[12:13]
	s_cbranch_vccz .LBB0_71
	s_cmp_lt_u32 s0, 0x18000
	s_cbranch_scc0 .LBB0_72
	s_addk_i32 s1, 0xdcff
	s_lshr_b32 s14, s1, 10
	s_mov_b32 s15, 0
	s_lshl_b64 s[2:3], s[14:15], 22
	s_lshl_b64 s[12:13], s[14:15], 24
	s_add_u32 s1, s70, s12
	s_addc_u32 s16, s71, s13
	s_add_u32 s2, s90, s2
	s_addc_u32 s3, s91, s3
	s_add_u32 s12, s2, 0x3b100000
	s_addc_u32 s13, s3, 0
	s_lshl_b32 s2, s0, 1
	s_and_b32 s14, s2, 0x780
	s_lshl_b32 s2, s14, 13
	s_add_u32 s1, s1, s2
	s_addc_u32 s2, s16, 0
	s_lshl_b32 s3, s0, 5
	s_and_b32 s18, s3, 0x7e0
	s_lshl_b32 s3, s18, 2
	s_add_u32 s16, s1, s3
	s_mov_b32 s19, s15
	s_addc_u32 s17, s2, 0
	s_mov_b64 s[20:21], 0
	s_branch .LBB0_73

.LBB0_77:
	s_lshl_b64 s[0:1], s[10:11], 11
	s_add_u32 s0, s4, s0
	s_addc_u32 s1, s5, s1
	s_add_u32 s8, s0, s8
	s_addc_u32 s9, s1, s9
	s_lshl_b64 s[2:3], s[18:19], 11
	s_add_u32 s0, s12, s2
	s_addc_u32 s2, s13, s3
	s_add_u32 s4, s0, s14
	v_mov_b32_e32 v49, 0
	s_addc_u32 s5, s2, s15
	v_mad_i64_i32 v[68:69], s[2:3], s20, v130, 0
	v_lshl_add_u64 v[68:69], v[68:69], 2, s[16:17]
	v_mov_b32_e32 v67, v49
	s_mov_b32 s1, 0
	v_lshl_add_u64 v[66:67], v[68:69], 0, v[66:67]
	s_lshl_b32 s0, s20, 2
	v_lshl_add_u64 v[68:69], v[66:67], 0, s[0:1]
	v_lshl_add_u64 v[66:67], v[68:69], 0, s[0:1]
	v_lshl_add_u64 v[68:69], v[66:67], 0, s[0:1]
	v_lshl_add_u64 v[66:67], v[68:69], 0, s[0:1]
	v_lshl_add_u64 v[68:69], v[66:67], 0, s[0:1]
	v_lshl_add_u64 v[66:67], v[68:69], 0, s[0:1]
	v_lshl_add_u64 v[68:69], v[66:67], 0, s[0:1]
	v_lshl_add_u64 v[66:67], v[68:69], 0, s[0:1]
	v_lshl_add_u64 v[66:67], v[66:67], 0, s[0:1]
	v_lshl_add_u64 v[66:67], v[66:67], 0, s[0:1]
	v_lshl_add_u64 v[66:67], v[66:67], 0, s[0:1]
	v_lshl_add_u64 v[66:67], v[66:67], 0, s[0:1]
	v_lshl_add_u64 v[66:67], v[66:67], 0, s[0:1]
	v_lshl_add_u64 v[70:71], v[66:67], 0, s[0:1]
	v_lshl_add_u64 v[70:71], v[70:71], 0, s[0:1]
	s_waitcnt vmcnt(13)
	v_mul_f32_e32 v8, 0x44000000, v8
	v_mul_f32_e32 v4, 0x44000000, v4
	v_mov_b32_e32 v135, v49
	v_cvt_pk_fp8_f32 v135, v8, v4
	v_mul_f32_e32 v0, 0x44000000, v0
	s_waitcnt vmcnt(1)
	v_mul_f32_e32 v4, 0x44000000, v24
	v_mov_b32_e32 v136, v49
	v_cvt_pk_fp8_f32 v135, v0, v4 op_sel:[0,0,1]
	s_waitcnt vmcnt(0)
	v_mul_f32_e32 v0, 0x44000000, v63
	v_mul_f32_e32 v4, 0x44000000, v59
	v_cvt_pk_fp8_f32 v136, v0, v4
	v_mul_f32_e32 v0, 0x44000000, v45
	v_mul_f32_e32 v4, 0x44000000, v41
	v_mov_b32_e32 v137, v49
	v_cvt_pk_fp8_f32 v137, v0, v4
	v_mul_f32_e32 v28, 0x44000000, v28
	v_mul_f32_e32 v20, 0x44000000, v20
	v_mov_b32_e32 v134, v49
	v_mul_f32_e32 v0, 0x44000000, v37
	v_mul_f32_e32 v4, 0x44000000, v33
	v_mul_f32_e32 v62, 0x44000000, v62
	v_mul_f32_e32 v58, 0x44000000, v58
	v_mov_b32_e32 v132, v49
	v_mul_f32_e32 v44, 0x44000000, v44
	v_mul_f32_e32 v40, 0x44000000, v40
	v_mov_b32_e32 v133, v49
	v_cvt_pk_fp8_f32 v134, v28, v20
	v_cvt_pk_fp8_f32 v137, v0, v4 op_sel:[0,0,1]
	v_mul_f32_e32 v0, 0x44000000, v29
	v_mul_f32_e32 v4, 0x44000000, v21
	v_mov_b32_e32 v138, v49
	v_cvt_pk_fp8_f32 v132, v62, v58
	v_cvt_pk_fp8_f32 v133, v44, v40
	v_cvt_pk_fp8_f32 v138, v0, v4
	v_mul_f32_e32 v0, 0x44000000, v9
	v_mul_f32_e32 v4, 0x44000000, v5
	v_mov_b32_e32 v139, v49
	v_cvt_pk_fp8_f32 v139, v0, v4
	v_mul_f32_e32 v16, 0x44000000, v16
	v_mul_f32_e32 v12, 0x44000000, v12
	v_mul_f32_e32 v54, 0x44000000, v54
	v_mul_f32_e32 v50, 0x44000000, v50
	v_mul_f32_e32 v36, 0x44000000, v36
	v_mul_f32_e32 v32, 0x44000000, v32
	v_cvt_pk_fp8_f32 v134, v16, v12 op_sel:[0,0,1]
	v_mul_f32_e32 v8, 0x44000000, v55
	v_mul_f32_e32 v12, 0x44000000, v51
	v_cvt_pk_fp8_f32 v132, v54, v50 op_sel:[0,0,1]
	v_cvt_pk_fp8_f32 v133, v36, v32 op_sel:[0,0,1]
	v_cvt_pk_fp8_f32 v136, v8, v12 op_sel:[0,0,1]
	v_mul_f32_e32 v8, 0x44000000, v17
	v_mul_f32_e32 v12, 0x44000000, v13
	v_mul_f32_e32 v0, 0x44000000, v1
	v_mul_f32_e32 v1, 0x44000000, v25
	v_lshlrev_b32_e32 v48, 11, v48
	v_cvt_pk_fp8_f32 v138, v8, v12 op_sel:[0,0,1]
	v_cvt_pk_fp8_f32 v139, v0, v1 op_sel:[0,0,1]
	v_lshl_add_u64 v[0:1], s[8:9], 0, v[48:49]
	v_lshl_add_u64 v[0:1], v[0:1], 0, v[130:131]
	global_store_dwordx4 v[0:1], v[132:135], off sc1 nt
	global_store_dwordx4 v[0:1], v[136:139], off offset:2048 sc1 nt
	v_mul_f32_e32 v4, 0x44000000, v64
	v_mul_f32_e32 v5, 0x44000000, v60
	v_mov_b32_e32 v132, v49
	v_cvt_pk_fp8_f32 v132, v4, v5
	v_mul_f32_e32 v4, 0x44000000, v46
	v_mul_f32_e32 v5, 0x44000000, v42
	v_mov_b32_e32 v133, v49
	v_cvt_pk_fp8_f32 v133, v4, v5
	v_mul_f32_e32 v4, 0x44000000, v38
	v_mul_f32_e32 v5, 0x44000000, v34
	v_mov_b32_e32 v134, v49
	v_cvt_pk_fp8_f32 v133, v4, v5 op_sel:[0,0,1]
	v_mul_f32_e32 v4, 0x44000000, v30
	v_mul_f32_e32 v5, 0x44000000, v22
	v_cvt_pk_fp8_f32 v134, v4, v5
	v_mul_f32_e32 v4, 0x44000000, v10
	v_mul_f32_e32 v5, 0x44000000, v6
	v_mov_b32_e32 v135, v49
	v_cvt_pk_fp8_f32 v135, v4, v5
	v_mul_f32_e32 v8, 0x44000000, v56
	v_mul_f32_e32 v9, 0x44000000, v52
	v_mul_f32_e32 v2, 0x44000000, v2
	v_mul_f32_e32 v4, 0x44000000, v26
	v_cvt_pk_fp8_f32 v132, v8, v9 op_sel:[0,0,1]
	v_mul_f32_e32 v8, 0x44000000, v18
	v_mul_f32_e32 v9, 0x44000000, v14
	v_cvt_pk_fp8_f32 v135, v2, v4 op_sel:[0,0,1]
	v_mul_f32_e32 v2, 0x44000000, v65
	v_mul_f32_e32 v5, 0x44000000, v61
	v_mov_b32_e32 v4, v49
	v_cvt_pk_fp8_f32 v134, v8, v9 op_sel:[0,0,1]
	v_cvt_pk_fp8_f32 v4, v2, v5
	v_mul_f32_e32 v2, 0x44000000, v47
	v_mul_f32_e32 v9, 0x44000000, v43
	v_mov_b32_e32 v5, v49
	v_cvt_pk_fp8_f32 v5, v2, v9
	v_mul_f32_e32 v6, 0x44000000, v57
	v_mul_f32_e32 v8, 0x44000000, v53
	v_cvt_pk_fp8_f32 v4, v6, v8 op_sel:[0,0,1]
	v_mul_f32_e32 v2, 0x44000000, v39
	v_mul_f32_e32 v6, 0x44000000, v35
	v_cvt_pk_fp8_f32 v5, v2, v6 op_sel:[0,0,1]
	v_mul_f32_e32 v2, 0x44000000, v31
	v_mul_f32_e32 v8, 0x44000000, v23
	v_mov_b32_e32 v6, v49
	v_cvt_pk_fp8_f32 v6, v2, v8
	v_mul_f32_e32 v2, 0x44000000, v11
	v_mul_f32_e32 v8, 0x44000000, v7
	v_mov_b32_e32 v7, v49
	v_cvt_pk_fp8_f32 v7, v2, v8
	v_mul_f32_e32 v9, 0x44000000, v19
	v_mul_f32_e32 v10, 0x44000000, v15
	v_mul_f32_e32 v2, 0x44000000, v3
	v_mul_f32_e32 v3, 0x44000000, v27
	s_movk_i32 s0, 0x1000
	v_cvt_pk_fp8_f32 v6, v9, v10 op_sel:[0,0,1]
	v_cvt_pk_fp8_f32 v7, v2, v3 op_sel:[0,0,1]
	v_add_co_u32_e32 v0, vcc, s0, v0
	s_waitcnt vmcnt(16)
	v_mul_f32_e32 v2, 0x44000000, v86
	v_addc_co_u32_e32 v1, vcc, 0, v1, vcc
	global_store_dwordx4 v[0:1], v[132:135], off sc1 nt
	global_store_dwordx4 v[0:1], v[4:7], off offset:2048 sc1 nt
	s_branch .Lside_done_0
	v_mul_f32_e32 v1, 0x44000000, v82
	v_mov_b32_e32 v0, v49
	v_cvt_pk_fp8_f32 v0, v1, v2
	s_waitcnt vmcnt(15)
	v_mul_f32_e32 v2, 0x44000000, v110
	s_waitcnt vmcnt(14)
	v_mul_f32_e32 v5, 0x44000000, v114
	v_mov_b32_e32 v1, v49
	v_cvt_pk_fp8_f32 v1, v2, v5
	v_mul_f32_e32 v3, 0x44000000, v122
	v_mul_f32_e32 v4, 0x44000000, v126
	v_cvt_pk_fp8_f32 v0, v3, v4 op_sel:[0,0,1]
	s_waitcnt vmcnt(13)
	v_mul_f32_e32 v2, 0x44000000, v90
	s_waitcnt vmcnt(12)
	v_mul_f32_e32 v3, 0x44000000, v94
	v_cvt_pk_fp8_f32 v1, v2, v3 op_sel:[0,0,1]
	s_waitcnt vmcnt(11)
	v_mul_f32_e32 v3, 0x44000000, v74
	s_waitcnt vmcnt(10)
	v_mul_f32_e32 v4, 0x44000000, v98
	v_mov_b32_e32 v2, v49
	v_cvt_pk_fp8_f32 v2, v3, v4
	s_waitcnt vmcnt(7)
	v_mul_f32_e32 v4, 0x44000000, v78
	s_waitcnt vmcnt(6)
	v_mul_f32_e32 v7, 0x44000000, v102
	v_mov_b32_e32 v3, v49
	v_cvt_pk_fp8_f32 v3, v4, v7
	v_mul_f32_e32 v5, 0x44000000, v106
	v_mul_f32_e32 v6, 0x44000000, v118
	v_cvt_pk_fp8_f32 v2, v5, v6 op_sel:[0,0,1]
	s_waitcnt vmcnt(5)
	v_mul_f32_e32 v4, 0x44000000, v66
	s_waitcnt vmcnt(4)
	v_mul_f32_e32 v5, 0x44000000, v70
	v_cvt_pk_fp8_f32 v3, v4, v5 op_sel:[0,0,1]
	v_mul_f32_e32 v5, 0x44000000, v83
	v_mul_f32_e32 v6, 0x44000000, v87
	v_mov_b32_e32 v4, v49
	v_cvt_pk_fp8_f32 v4, v5, v6
	v_mul_f32_e32 v6, 0x44000000, v111
	v_mul_f32_e32 v9, 0x44000000, v115
	v_mov_b32_e32 v5, v49
	v_cvt_pk_fp8_f32 v5, v6, v9
	v_mul_f32_e32 v7, 0x44000000, v123
	v_mul_f32_e32 v8, 0x44000000, v127
	v_cvt_pk_fp8_f32 v4, v7, v8 op_sel:[0,0,1]
	v_mul_f32_e32 v6, 0x44000000, v91
	v_mul_f32_e32 v7, 0x44000000, v95
	v_cvt_pk_fp8_f32 v5, v6, v7 op_sel:[0,0,1]
	v_mul_f32_e32 v7, 0x44000000, v75
	v_mul_f32_e32 v8, 0x44000000, v99
	v_mov_b32_e32 v6, v49
	v_cvt_pk_fp8_f32 v6, v7, v8
	v_mul_f32_e32 v8, 0x44000000, v79
	v_mul_f32_e32 v11, 0x44000000, v103
	v_mov_b32_e32 v7, v49
	v_cvt_pk_fp8_f32 v7, v8, v11
	v_mul_f32_e32 v9, 0x44000000, v107
	v_mul_f32_e32 v10, 0x44000000, v119
	v_cvt_pk_fp8_f32 v6, v9, v10 op_sel:[0,0,1]
	v_mul_f32_e32 v8, 0x44000000, v67
	v_mul_f32_e32 v9, 0x44000000, v71
	v_cvt_pk_fp8_f32 v7, v8, v9 op_sel:[0,0,1]
	v_lshl_add_u64 v[8:9], s[4:5], 0, v[48:49]
	v_lshl_add_u64 v[8:9], v[8:9], 0, v[130:131]
	global_store_dwordx4 v[8:9], v[0:3], off sc1 nt
	global_store_dwordx4 v[8:9], v[4:7], off offset:2048 sc1 nt
	v_mov_b32_e32 v46, v49
	v_mul_f32_e32 v1, 0x44000000, v84
	v_mul_f32_e32 v2, 0x44000000, v88
	v_mov_b32_e32 v0, v49
	v_cvt_pk_fp8_f32 v0, v1, v2
	v_mul_f32_e32 v2, 0x44000000, v112
	v_mul_f32_e32 v5, 0x44000000, v116
	v_mov_b32_e32 v1, v49
	v_cvt_pk_fp8_f32 v1, v2, v5
	v_mul_f32_e32 v3, 0x44000000, v124
	v_mul_f32_e32 v4, 0x44000000, v128
	v_cvt_pk_fp8_f32 v0, v3, v4 op_sel:[0,0,1]
	v_mul_f32_e32 v2, 0x44000000, v92
	v_mul_f32_e32 v3, 0x44000000, v96
	v_cvt_pk_fp8_f32 v1, v2, v3 op_sel:[0,0,1]
	v_mul_f32_e32 v3, 0x44000000, v76
	v_mul_f32_e32 v4, 0x44000000, v100
	v_mov_b32_e32 v2, v49
	v_cvt_pk_fp8_f32 v2, v3, v4
	v_mul_f32_e32 v4, 0x44000000, v80
	v_mul_f32_e32 v7, 0x44000000, v104
	v_mov_b32_e32 v3, v49
	v_cvt_pk_fp8_f32 v3, v4, v7
	v_mul_f32_e32 v5, 0x44000000, v108
	v_mul_f32_e32 v6, 0x44000000, v120
	v_cvt_pk_fp8_f32 v2, v5, v6 op_sel:[0,0,1]
	v_mul_f32_e32 v4, 0x44000000, v68
	v_mul_f32_e32 v5, 0x44000000, v72
	v_cvt_pk_fp8_f32 v3, v4, v5 op_sel:[0,0,1]
	v_mul_f32_e32 v4, 0x44000000, v85
	v_mul_f32_e32 v5, 0x44000000, v89
	v_cvt_pk_fp8_f32 v46, v4, v5
	v_mul_f32_e32 v4, 0x44000000, v113
	v_mul_f32_e32 v5, 0x44000000, v117
	v_mov_b32_e32 v47, v49
	v_cvt_pk_fp8_f32 v47, v4, v5
	v_mul_f32_e32 v4, 0x44000000, v93
	v_mul_f32_e32 v5, 0x44000000, v97
	v_mov_b32_e32 v48, v49
	v_cvt_pk_fp8_f32 v47, v4, v5 op_sel:[0,0,1]
	v_mul_f32_e32 v4, 0x44000000, v77
	v_mul_f32_e32 v5, 0x44000000, v101
	v_cvt_pk_fp8_f32 v48, v4, v5
	v_mul_f32_e32 v4, 0x44000000, v81
	v_mul_f32_e32 v5, 0x44000000, v105
	v_cvt_pk_fp8_f32 v49, v4, v5
	v_mul_f32_e32 v6, 0x44000000, v125
	v_mul_f32_e32 v7, 0x44000000, v129
	v_cvt_pk_fp8_f32 v46, v6, v7 op_sel:[0,0,1]
	v_mul_f32_e32 v6, 0x44000000, v109
	v_mul_f32_e32 v7, 0x44000000, v121
	v_mul_f32_e32 v4, 0x44000000, v69
	v_mul_f32_e32 v5, 0x44000000, v73
	v_cvt_pk_fp8_f32 v48, v6, v7 op_sel:[0,0,1]
	v_cvt_pk_fp8_f32 v49, v4, v5 op_sel:[0,0,1]
	v_add_co_u32_e32 v4, vcc, s0, v8
	s_nop 1
	v_addc_co_u32_e32 v5, vcc, 0, v9, vcc
	global_store_dwordx4 v[4:5], v[0:3], off sc1 nt
	global_store_dwordx4 v[4:5], v[46:49], off offset:2048 sc1 nt
.Lside_done_0:
	s_waitcnt vmcnt(0)
.LBB0_78:
	s_mov_b64 s[4:5], 0

.LBB0_296:
	s_cmp_gt_i32 s95, 2
	s_cselect_b64 s[4:5], -1, 0
	s_and_b64 s[0:1], s[22:23], s[4:5]
	v_readlane_b32 s86, v255, 26
	s_andn2_b64 vcc, exec, s[0:1]
	v_readlane_b32 s87, v255, 27
	s_cbranch_vccnz .LBB0_374
	s_waitcnt vmcnt(0)
	v_readlane_b32 s0, v255, 0
	s_cmp_gt_u32 s0, 63
	s_mov_b64 s[6:7], -1
	s_barrier
	s_cbranch_scc0 .LBB0_319
	v_readlane_b32 s0, v255, 0
	s_cmpk_gt_u32 s0, 0x1ff
	s_cbranch_scc1 .LBB0_318
	v_readlane_b32 s0, v255, 4
	s_mul_i32 s1, s0, 7
	v_readlane_b32 s0, v255, 28
	s_add_i32 s1, s1, s0
	s_add_i32 s0, s1, 0xe3ff
	s_cmp_gt_i32 s0, 0xffff
	s_cselect_b64 s[12:13], -1, 0
	s_and_b64 vcc, exec, s[12:13]
	s_waitcnt vmcnt(5)
	v_mbcnt_lo_u32_b32 v0, -1, 0
	v_mbcnt_hi_u32_b32 v0, -1, v0
	s_cbranch_vccz .LBB0_302
	s_cmp_lt_u32 s0, 0x18000
	s_cbranch_scc0 .LBB0_303
	s_add_i32 s2, s1, 0xffffe3ff
	s_lshr_b32 s8, s2, 10
	s_mov_b32 s9, 0
	s_lshl_b64 s[2:3], s[8:9], 22
	s_lshl_b64 s[6:7], s[8:9], 24
	s_add_u32 s10, s70, s6
	s_addc_u32 s11, s71, s7
	s_add_u32 s2, s90, s2
	s_addc_u32 s3, s91, s3
	s_add_u32 s6, s2, 0x3b100000
	s_addc_u32 s7, s3, 0
	s_lshl_b32 s2, s0, 1
	s_and_b32 s8, s2, 0x780
	s_lshl_b32 s2, s8, 13
	s_add_u32 s2, s10, s2
	s_addc_u32 s3, s11, 0
	s_lshl_b32 s10, s0, 5
	s_and_b32 s10, s10, 0x7e0
	s_lshl_b32 s14, s10, 2
	s_add_u32 s14, s2, s14
	s_mov_b32 s11, s9
	s_addc_u32 s15, s3, 0
	s_mov_b64 s[16:17], 0
	s_branch .LBB0_304

.LBB0_308:
	v_lshlrev_b32_e32 v1, 1, v0
	v_and_b32_e32 v130, -16, v1
	v_lshlrev_b32_e32 v0, 2, v0
	v_and_b32_e32 v48, 28, v0
	v_mad_i64_i32 v[0:1], s[18:19], s16, v130, 0
	v_mov_b32_e32 v67, 0
	v_lshl_add_u64 v[0:1], v[0:1], 2, s[14:15]
	v_lshlrev_b32_e32 v66, 2, v48
	s_mov_b32 s3, 0
	v_lshl_add_u64 v[62:63], v[0:1], 0, v[66:67]
	s_mul_i32 s2, s16, 60
	v_lshl_add_u64 v[24:25], v[62:63], 0, s[2:3]
	s_lshl_b32 s2, s16, 2
	s_sub_u32 s2, 0, s2
	s_subb_u32 s3, 0, 0
	v_lshl_add_u64 v[0:1], v[24:25], 0, s[2:3]
	v_lshl_add_u64 v[8:9], v[0:1], 0, s[2:3]
	global_load_dwordx4 v[0:3], v[0:1], off sc1 nt
	s_nop 0
	global_load_dwordx4 v[4:7], v[8:9], off sc1 nt
	v_lshl_add_u64 v[8:9], v[8:9], 0, s[2:3]
	v_lshl_add_u64 v[16:17], v[8:9], 0, s[2:3]
	global_load_dwordx4 v[8:11], v[8:9], off sc1 nt
	s_nop 0
	global_load_dwordx4 v[12:15], v[16:17], off sc1 nt
	v_lshl_add_u64 v[16:17], v[16:17], 0, s[2:3]
	v_lshl_add_u64 v[26:27], v[16:17], 0, s[2:3]
	global_load_dwordx4 v[16:19], v[16:17], off sc1 nt
	s_nop 0
	global_load_dwordx4 v[20:23], v[26:27], off sc1 nt
	v_lshl_add_u64 v[26:27], v[26:27], 0, s[2:3]
	global_load_dwordx4 v[28:31], v[26:27], off sc1 nt
	v_lshl_add_u64 v[26:27], v[26:27], 0, s[2:3]
	global_load_dwordx4 v[32:35], v[26:27], off sc1 nt
	v_lshl_add_u64 v[26:27], v[26:27], 0, s[2:3]
	global_load_dwordx4 v[36:39], v[26:27], off sc1 nt
	v_lshl_add_u64 v[26:27], v[26:27], 0, s[2:3]
	global_load_dwordx4 v[40:43], v[26:27], off sc1 nt
	v_lshl_add_u64 v[26:27], v[26:27], 0, s[2:3]
	global_load_dwordx4 v[44:47], v[26:27], off sc1 nt
	v_lshl_add_u64 v[26:27], v[26:27], 0, s[2:3]
	global_load_dwordx4 v[50:53], v[26:27], off sc1 nt
	v_lshl_add_u64 v[26:27], v[26:27], 0, s[2:3]
	global_load_dwordx4 v[54:57], v[26:27], off sc1 nt
	v_lshl_add_u64 v[26:27], v[26:27], 0, s[2:3]
	global_load_dwordx4 v[58:61], v[26:27], off sc1 nt
	s_nop 0
	global_load_dwordx4 v[24:27], v[24:25], off sc1 nt
	s_nop 0
	global_load_dwordx4 v[62:65], v[62:63], off sc1 nt
	v_ashrrev_i32_e32 v131, 31, v130
	s_and_b64 vcc, exec, s[12:13]
	s_cbranch_vccz .LBB0_311
	s_cmp_lt_u32 s0, 0x18000
	s_cbranch_scc0 .LBB0_312
	s_addk_i32 s1, 0xe3ff
	s_lshr_b32 s14, s1, 10
	s_mov_b32 s15, 0
	s_lshl_b64 s[2:3], s[14:15], 22
	s_lshl_b64 s[12:13], s[14:15], 24
	s_add_u32 s1, s70, s12
	s_addc_u32 s16, s71, s13
	s_add_u32 s2, s90, s2
	s_addc_u32 s3, s91, s3
	s_add_u32 s12, s2, 0x3b100000
	s_addc_u32 s13, s3, 0
	s_lshl_b32 s2, s0, 1
	s_and_b32 s14, s2, 0x780
	s_lshl_b32 s2, s14, 13
	s_add_u32 s1, s1, s2
	s_addc_u32 s2, s16, 0
	s_lshl_b32 s3, s0, 5
	s_and_b32 s18, s3, 0x7e0
	s_lshl_b32 s3, s18, 2
	s_add_u32 s16, s1, s3
	s_mov_b32 s19, s15
	s_addc_u32 s17, s2, 0
	s_mov_b64 s[20:21], 0
	s_branch .LBB0_313

.LBB0_317:
	s_lshl_b64 s[0:1], s[10:11], 11
	s_add_u32 s0, s6, s0
	s_addc_u32 s1, s7, s1
	s_add_u32 s8, s0, s8
	s_addc_u32 s9, s1, s9
	s_lshl_b64 s[2:3], s[18:19], 11
	s_add_u32 s0, s12, s2
	s_addc_u32 s2, s13, s3
	s_add_u32 s6, s0, s14
	v_mov_b32_e32 v49, 0
	s_addc_u32 s7, s2, s15
	v_mad_i64_i32 v[68:69], s[2:3], s20, v130, 0
	v_lshl_add_u64 v[68:69], v[68:69], 2, s[16:17]
	v_mov_b32_e32 v67, v49
	s_mov_b32 s1, 0
	v_lshl_add_u64 v[66:67], v[68:69], 0, v[66:67]
	s_lshl_b32 s0, s20, 2
	v_lshl_add_u64 v[68:69], v[66:67], 0, s[0:1]
	v_lshl_add_u64 v[66:67], v[68:69], 0, s[0:1]
	v_lshl_add_u64 v[68:69], v[66:67], 0, s[0:1]
	v_lshl_add_u64 v[66:67], v[68:69], 0, s[0:1]
	v_lshl_add_u64 v[68:69], v[66:67], 0, s[0:1]
	v_lshl_add_u64 v[66:67], v[68:69], 0, s[0:1]
	v_lshl_add_u64 v[68:69], v[66:67], 0, s[0:1]
	v_lshl_add_u64 v[66:67], v[68:69], 0, s[0:1]
	v_lshl_add_u64 v[66:67], v[66:67], 0, s[0:1]
	v_lshl_add_u64 v[66:67], v[66:67], 0, s[0:1]
	v_lshl_add_u64 v[66:67], v[66:67], 0, s[0:1]
	v_lshl_add_u64 v[66:67], v[66:67], 0, s[0:1]
	v_lshl_add_u64 v[66:67], v[66:67], 0, s[0:1]
	v_lshl_add_u64 v[70:71], v[66:67], 0, s[0:1]
	v_lshl_add_u64 v[70:71], v[70:71], 0, s[0:1]
	s_waitcnt vmcnt(13)
	v_mul_f32_e32 v8, 0x44000000, v8
	v_mul_f32_e32 v4, 0x44000000, v4
	v_mov_b32_e32 v135, v49
	v_cvt_pk_fp8_f32 v135, v8, v4
	v_mul_f32_e32 v0, 0x44000000, v0
	s_waitcnt vmcnt(1)
	v_mul_f32_e32 v4, 0x44000000, v24
	v_mov_b32_e32 v136, v49
	v_cvt_pk_fp8_f32 v135, v0, v4 op_sel:[0,0,1]
	s_waitcnt vmcnt(0)
	v_mul_f32_e32 v0, 0x44000000, v63
	v_mul_f32_e32 v4, 0x44000000, v59
	v_cvt_pk_fp8_f32 v136, v0, v4
	v_mul_f32_e32 v0, 0x44000000, v45
	v_mul_f32_e32 v4, 0x44000000, v41
	v_mov_b32_e32 v137, v49
	v_cvt_pk_fp8_f32 v137, v0, v4
	v_mul_f32_e32 v28, 0x44000000, v28
	v_mul_f32_e32 v20, 0x44000000, v20
	v_mov_b32_e32 v134, v49
	v_mul_f32_e32 v0, 0x44000000, v37
	v_mul_f32_e32 v4, 0x44000000, v33
	v_mul_f32_e32 v62, 0x44000000, v62
	v_mul_f32_e32 v58, 0x44000000, v58
	v_mov_b32_e32 v132, v49
	v_mul_f32_e32 v44, 0x44000000, v44
	v_mul_f32_e32 v40, 0x44000000, v40
	v_mov_b32_e32 v133, v49
	v_cvt_pk_fp8_f32 v134, v28, v20
	v_cvt_pk_fp8_f32 v137, v0, v4 op_sel:[0,0,1]
	v_mul_f32_e32 v0, 0x44000000, v29
	v_mul_f32_e32 v4, 0x44000000, v21
	v_mov_b32_e32 v138, v49
	v_cvt_pk_fp8_f32 v132, v62, v58
	v_cvt_pk_fp8_f32 v133, v44, v40
	v_cvt_pk_fp8_f32 v138, v0, v4
	v_mul_f32_e32 v0, 0x44000000, v9
	v_mul_f32_e32 v4, 0x44000000, v5
	v_mov_b32_e32 v139, v49
	v_cvt_pk_fp8_f32 v139, v0, v4
	v_mul_f32_e32 v16, 0x44000000, v16
	v_mul_f32_e32 v12, 0x44000000, v12
	v_mul_f32_e32 v54, 0x44000000, v54
	v_mul_f32_e32 v50, 0x44000000, v50
	v_mul_f32_e32 v36, 0x44000000, v36
	v_mul_f32_e32 v32, 0x44000000, v32
	v_cvt_pk_fp8_f32 v134, v16, v12 op_sel:[0,0,1]
	v_mul_f32_e32 v8, 0x44000000, v55
	v_mul_f32_e32 v12, 0x44000000, v51
	v_cvt_pk_fp8_f32 v132, v54, v50 op_sel:[0,0,1]
	v_cvt_pk_fp8_f32 v133, v36, v32 op_sel:[0,0,1]
	v_cvt_pk_fp8_f32 v136, v8, v12 op_sel:[0,0,1]
	v_mul_f32_e32 v8, 0x44000000, v17
	v_mul_f32_e32 v12, 0x44000000, v13
	v_mul_f32_e32 v0, 0x44000000, v1
	v_mul_f32_e32 v1, 0x44000000, v25
	v_lshlrev_b32_e32 v48, 11, v48
	v_cvt_pk_fp8_f32 v138, v8, v12 op_sel:[0,0,1]
	v_cvt_pk_fp8_f32 v139, v0, v1 op_sel:[0,0,1]
	v_lshl_add_u64 v[0:1], s[8:9], 0, v[48:49]
	v_lshl_add_u64 v[0:1], v[0:1], 0, v[130:131]
	global_store_dwordx4 v[0:1], v[132:135], off sc1 nt
	global_store_dwordx4 v[0:1], v[136:139], off offset:2048 sc1 nt
	v_mul_f32_e32 v4, 0x44000000, v64
	v_mul_f32_e32 v5, 0x44000000, v60
	v_mov_b32_e32 v132, v49
	v_cvt_pk_fp8_f32 v132, v4, v5
	v_mul_f32_e32 v4, 0x44000000, v46
	v_mul_f32_e32 v5, 0x44000000, v42
	v_mov_b32_e32 v133, v49
	v_cvt_pk_fp8_f32 v133, v4, v5
	v_mul_f32_e32 v4, 0x44000000, v38
	v_mul_f32_e32 v5, 0x44000000, v34
	v_mov_b32_e32 v134, v49
	v_cvt_pk_fp8_f32 v133, v4, v5 op_sel:[0,0,1]
	v_mul_f32_e32 v4, 0x44000000, v30
	v_mul_f32_e32 v5, 0x44000000, v22
	v_cvt_pk_fp8_f32 v134, v4, v5
	v_mul_f32_e32 v4, 0x44000000, v10
	v_mul_f32_e32 v5, 0x44000000, v6
	v_mov_b32_e32 v135, v49
	v_cvt_pk_fp8_f32 v135, v4, v5
	v_mul_f32_e32 v8, 0x44000000, v56
	v_mul_f32_e32 v9, 0x44000000, v52
	v_mul_f32_e32 v2, 0x44000000, v2
	v_mul_f32_e32 v4, 0x44000000, v26
	v_cvt_pk_fp8_f32 v132, v8, v9 op_sel:[0,0,1]
	v_mul_f32_e32 v8, 0x44000000, v18
	v_mul_f32_e32 v9, 0x44000000, v14
	v_cvt_pk_fp8_f32 v135, v2, v4 op_sel:[0,0,1]
	v_mul_f32_e32 v2, 0x44000000, v65
	v_mul_f32_e32 v5, 0x44000000, v61
	v_mov_b32_e32 v4, v49
	v_cvt_pk_fp8_f32 v134, v8, v9 op_sel:[0,0,1]
	v_cvt_pk_fp8_f32 v4, v2, v5
	v_mul_f32_e32 v2, 0x44000000, v47
	v_mul_f32_e32 v9, 0x44000000, v43
	v_mov_b32_e32 v5, v49
	v_cvt_pk_fp8_f32 v5, v2, v9
	v_mul_f32_e32 v6, 0x44000000, v57
	v_mul_f32_e32 v8, 0x44000000, v53
	v_cvt_pk_fp8_f32 v4, v6, v8 op_sel:[0,0,1]
	v_mul_f32_e32 v2, 0x44000000, v39
	v_mul_f32_e32 v6, 0x44000000, v35
	v_cvt_pk_fp8_f32 v5, v2, v6 op_sel:[0,0,1]
	v_mul_f32_e32 v2, 0x44000000, v31
	v_mul_f32_e32 v8, 0x44000000, v23
	v_mov_b32_e32 v6, v49
	v_cvt_pk_fp8_f32 v6, v2, v8
	v_mul_f32_e32 v2, 0x44000000, v11
	v_mul_f32_e32 v8, 0x44000000, v7
	v_mov_b32_e32 v7, v49
	v_cvt_pk_fp8_f32 v7, v2, v8
	v_mul_f32_e32 v9, 0x44000000, v19
	v_mul_f32_e32 v10, 0x44000000, v15
	v_mul_f32_e32 v2, 0x44000000, v3
	v_mul_f32_e32 v3, 0x44000000, v27
	s_movk_i32 s0, 0x1000
	v_cvt_pk_fp8_f32 v6, v9, v10 op_sel:[0,0,1]
	v_cvt_pk_fp8_f32 v7, v2, v3 op_sel:[0,0,1]
	v_add_co_u32_e32 v0, vcc, s0, v0
	s_waitcnt vmcnt(16)
	v_mul_f32_e32 v2, 0x44000000, v86
	v_addc_co_u32_e32 v1, vcc, 0, v1, vcc
	global_store_dwordx4 v[0:1], v[132:135], off sc1 nt
	global_store_dwordx4 v[0:1], v[4:7], off offset:2048 sc1 nt
	s_branch .Lside_done_1
	v_mul_f32_e32 v1, 0x44000000, v82
	v_mov_b32_e32 v0, v49
	v_cvt_pk_fp8_f32 v0, v1, v2
	s_waitcnt vmcnt(15)
	v_mul_f32_e32 v2, 0x44000000, v110
	s_waitcnt vmcnt(14)
	v_mul_f32_e32 v5, 0x44000000, v114
	v_mov_b32_e32 v1, v49
	v_cvt_pk_fp8_f32 v1, v2, v5
	v_mul_f32_e32 v3, 0x44000000, v122
	v_mul_f32_e32 v4, 0x44000000, v126
	v_cvt_pk_fp8_f32 v0, v3, v4 op_sel:[0,0,1]
	s_waitcnt vmcnt(13)
	v_mul_f32_e32 v2, 0x44000000, v90
	s_waitcnt vmcnt(12)
	v_mul_f32_e32 v3, 0x44000000, v94
	v_cvt_pk_fp8_f32 v1, v2, v3 op_sel:[0,0,1]
	s_waitcnt vmcnt(11)
	v_mul_f32_e32 v3, 0x44000000, v74
	s_waitcnt vmcnt(10)
	v_mul_f32_e32 v4, 0x44000000, v98
	v_mov_b32_e32 v2, v49
	v_cvt_pk_fp8_f32 v2, v3, v4
	s_waitcnt vmcnt(7)
	v_mul_f32_e32 v4, 0x44000000, v78
	s_waitcnt vmcnt(6)
	v_mul_f32_e32 v7, 0x44000000, v102
	v_mov_b32_e32 v3, v49
	v_cvt_pk_fp8_f32 v3, v4, v7
	v_mul_f32_e32 v5, 0x44000000, v106
	v_mul_f32_e32 v6, 0x44000000, v118
	v_cvt_pk_fp8_f32 v2, v5, v6 op_sel:[0,0,1]
	s_waitcnt vmcnt(5)
	v_mul_f32_e32 v4, 0x44000000, v66
	s_waitcnt vmcnt(4)
	v_mul_f32_e32 v5, 0x44000000, v70
	v_cvt_pk_fp8_f32 v3, v4, v5 op_sel:[0,0,1]
	v_mul_f32_e32 v5, 0x44000000, v83
	v_mul_f32_e32 v6, 0x44000000, v87
	v_mov_b32_e32 v4, v49
	v_cvt_pk_fp8_f32 v4, v5, v6
	v_mul_f32_e32 v6, 0x44000000, v111
	v_mul_f32_e32 v9, 0x44000000, v115
	v_mov_b32_e32 v5, v49
	v_cvt_pk_fp8_f32 v5, v6, v9
	v_mul_f32_e32 v7, 0x44000000, v123
	v_mul_f32_e32 v8, 0x44000000, v127
	v_cvt_pk_fp8_f32 v4, v7, v8 op_sel:[0,0,1]
	v_mul_f32_e32 v6, 0x44000000, v91
	v_mul_f32_e32 v7, 0x44000000, v95
	v_cvt_pk_fp8_f32 v5, v6, v7 op_sel:[0,0,1]
	v_mul_f32_e32 v7, 0x44000000, v75
	v_mul_f32_e32 v8, 0x44000000, v99
	v_mov_b32_e32 v6, v49
	v_cvt_pk_fp8_f32 v6, v7, v8
	v_mul_f32_e32 v8, 0x44000000, v79
	v_mul_f32_e32 v11, 0x44000000, v103
	v_mov_b32_e32 v7, v49
	v_cvt_pk_fp8_f32 v7, v8, v11
	v_mul_f32_e32 v9, 0x44000000, v107
	v_mul_f32_e32 v10, 0x44000000, v119
	v_cvt_pk_fp8_f32 v6, v9, v10 op_sel:[0,0,1]
	v_mul_f32_e32 v8, 0x44000000, v67
	v_mul_f32_e32 v9, 0x44000000, v71
	v_cvt_pk_fp8_f32 v7, v8, v9 op_sel:[0,0,1]
	v_lshl_add_u64 v[8:9], s[6:7], 0, v[48:49]
	v_lshl_add_u64 v[8:9], v[8:9], 0, v[130:131]
	global_store_dwordx4 v[8:9], v[0:3], off sc1 nt
	global_store_dwordx4 v[8:9], v[4:7], off offset:2048 sc1 nt
	v_mov_b32_e32 v46, v49
	v_mul_f32_e32 v1, 0x44000000, v84
	v_mul_f32_e32 v2, 0x44000000, v88
	v_mov_b32_e32 v0, v49
	v_cvt_pk_fp8_f32 v0, v1, v2
	v_mul_f32_e32 v2, 0x44000000, v112
	v_mul_f32_e32 v5, 0x44000000, v116
	v_mov_b32_e32 v1, v49
	v_cvt_pk_fp8_f32 v1, v2, v5
	v_mul_f32_e32 v3, 0x44000000, v124
	v_mul_f32_e32 v4, 0x44000000, v128
	v_cvt_pk_fp8_f32 v0, v3, v4 op_sel:[0,0,1]
	v_mul_f32_e32 v2, 0x44000000, v92
	v_mul_f32_e32 v3, 0x44000000, v96
	v_cvt_pk_fp8_f32 v1, v2, v3 op_sel:[0,0,1]
	v_mul_f32_e32 v3, 0x44000000, v76
	v_mul_f32_e32 v4, 0x44000000, v100
	v_mov_b32_e32 v2, v49
	v_cvt_pk_fp8_f32 v2, v3, v4
	v_mul_f32_e32 v4, 0x44000000, v80
	v_mul_f32_e32 v7, 0x44000000, v104
	v_mov_b32_e32 v3, v49
	v_cvt_pk_fp8_f32 v3, v4, v7
	v_mul_f32_e32 v5, 0x44000000, v108
	v_mul_f32_e32 v6, 0x44000000, v120
	v_cvt_pk_fp8_f32 v2, v5, v6 op_sel:[0,0,1]
	v_mul_f32_e32 v4, 0x44000000, v68
	v_mul_f32_e32 v5, 0x44000000, v72
	v_cvt_pk_fp8_f32 v3, v4, v5 op_sel:[0,0,1]
	v_mul_f32_e32 v4, 0x44000000, v85
	v_mul_f32_e32 v5, 0x44000000, v89
	v_cvt_pk_fp8_f32 v46, v4, v5
	v_mul_f32_e32 v4, 0x44000000, v113
	v_mul_f32_e32 v5, 0x44000000, v117
	v_mov_b32_e32 v47, v49
	v_cvt_pk_fp8_f32 v47, v4, v5
	v_mul_f32_e32 v4, 0x44000000, v93
	v_mul_f32_e32 v5, 0x44000000, v97
	v_mov_b32_e32 v48, v49
	v_cvt_pk_fp8_f32 v47, v4, v5 op_sel:[0,0,1]
	v_mul_f32_e32 v4, 0x44000000, v77
	v_mul_f32_e32 v5, 0x44000000, v101
	v_cvt_pk_fp8_f32 v48, v4, v5
	v_mul_f32_e32 v4, 0x44000000, v81
	v_mul_f32_e32 v5, 0x44000000, v105
	v_cvt_pk_fp8_f32 v49, v4, v5
	v_mul_f32_e32 v6, 0x44000000, v125
	v_mul_f32_e32 v7, 0x44000000, v129
	v_cvt_pk_fp8_f32 v46, v6, v7 op_sel:[0,0,1]
	v_mul_f32_e32 v6, 0x44000000, v109
	v_mul_f32_e32 v7, 0x44000000, v121
	v_mul_f32_e32 v4, 0x44000000, v69
	v_mul_f32_e32 v5, 0x44000000, v73
	v_cvt_pk_fp8_f32 v48, v6, v7 op_sel:[0,0,1]
	v_cvt_pk_fp8_f32 v49, v4, v5 op_sel:[0,0,1]
	v_add_co_u32_e32 v4, vcc, s0, v8
	s_nop 1
	v_addc_co_u32_e32 v5, vcc, 0, v9, vcc
	global_store_dwordx4 v[4:5], v[0:3], off sc1 nt
	global_store_dwordx4 v[4:5], v[46:49], off offset:2048 sc1 nt
.Lside_done_1:
	s_waitcnt vmcnt(0)
.LBB0_318:
	s_mov_b64 s[6:7], 0

.LBB0_387:
	s_cmp_gt_u32 s95, 3
	s_cselect_b64 s[0:1], -1, 0
	s_and_b64 s[0:1], s[56:57], s[0:1]
	s_andn2_b64 vcc, exec, s[0:1]
	s_cbranch_vccnz .LBB0_465
	s_waitcnt vmcnt(0)
	v_readlane_b32 s0, v255, 0
	s_cmp_gt_u32 s0, 63
	s_mov_b64 s[4:5], -1
	s_barrier
	s_cbranch_scc0 .LBB0_410
	v_readlane_b32 s0, v255, 0
	s_cmpk_gt_u32 s0, 0x1ff
	s_cbranch_scc1 .LBB0_409
	v_readlane_b32 s0, v255, 4
	s_mul_i32 s1, s0, 7
	v_readlane_b32 s0, v255, 28
	s_add_i32 s1, s1, s0
	s_add_i32 s0, s1, 0xeaff
	s_cmp_gt_i32 s0, 0xffff
	s_cselect_b64 s[10:11], -1, 0
	s_and_b64 vcc, exec, s[10:11]
	s_waitcnt vmcnt(5)
	v_mbcnt_lo_u32_b32 v0, -1, 0
	v_mbcnt_hi_u32_b32 v0, -1, v0
	s_cbranch_vccz .LBB0_393
	s_cmp_lt_u32 s0, 0x18000
	s_cbranch_scc0 .LBB0_394
	s_add_i32 s2, s1, 0xffffeaff
	s_lshr_b32 s6, s2, 10
	s_mov_b32 s7, 0
	s_lshl_b64 s[2:3], s[6:7], 22
	s_lshl_b64 s[4:5], s[6:7], 24
	s_add_u32 s8, s70, s4
	s_addc_u32 s9, s71, s5
	s_add_u32 s2, s90, s2
	s_addc_u32 s3, s91, s3
	s_add_u32 s4, s2, 0x3b100000
	s_addc_u32 s5, s3, 0
	s_lshl_b32 s2, s0, 1
	s_and_b32 s6, s2, 0x780
	s_lshl_b32 s2, s6, 13
	s_add_u32 s2, s8, s2
	s_addc_u32 s3, s9, 0
	s_lshl_b32 s8, s0, 5
	s_and_b32 s8, s8, 0x7e0
	s_lshl_b32 s12, s8, 2
	s_add_u32 s12, s2, s12
	s_mov_b32 s9, s7
	s_addc_u32 s13, s3, 0
	s_mov_b64 s[14:15], 0
	s_branch .LBB0_395

.LBB0_399:
	v_lshlrev_b32_e32 v1, 1, v0
	v_and_b32_e32 v130, -16, v1
	v_lshlrev_b32_e32 v0, 2, v0
	v_and_b32_e32 v48, 28, v0
	v_mad_i64_i32 v[0:1], s[16:17], s14, v130, 0
	v_mov_b32_e32 v67, 0
	v_lshl_add_u64 v[0:1], v[0:1], 2, s[12:13]
	v_lshlrev_b32_e32 v66, 2, v48
	s_mov_b32 s3, 0
	v_lshl_add_u64 v[62:63], v[0:1], 0, v[66:67]
	s_mul_i32 s2, s14, 60
	v_lshl_add_u64 v[24:25], v[62:63], 0, s[2:3]
	s_lshl_b32 s2, s14, 2
	s_sub_u32 s2, 0, s2
	s_subb_u32 s3, 0, 0
	v_lshl_add_u64 v[0:1], v[24:25], 0, s[2:3]
	v_lshl_add_u64 v[8:9], v[0:1], 0, s[2:3]
	global_load_dwordx4 v[0:3], v[0:1], off sc1 nt
	s_nop 0
	global_load_dwordx4 v[4:7], v[8:9], off sc1 nt
	v_lshl_add_u64 v[8:9], v[8:9], 0, s[2:3]
	v_lshl_add_u64 v[16:17], v[8:9], 0, s[2:3]
	global_load_dwordx4 v[8:11], v[8:9], off sc1 nt
	s_nop 0
	global_load_dwordx4 v[12:15], v[16:17], off sc1 nt
	v_lshl_add_u64 v[16:17], v[16:17], 0, s[2:3]
	v_lshl_add_u64 v[26:27], v[16:17], 0, s[2:3]
	global_load_dwordx4 v[16:19], v[16:17], off sc1 nt
	s_nop 0
	global_load_dwordx4 v[20:23], v[26:27], off sc1 nt
	v_lshl_add_u64 v[26:27], v[26:27], 0, s[2:3]
	global_load_dwordx4 v[28:31], v[26:27], off sc1 nt
	v_lshl_add_u64 v[26:27], v[26:27], 0, s[2:3]
	global_load_dwordx4 v[32:35], v[26:27], off sc1 nt
	v_lshl_add_u64 v[26:27], v[26:27], 0, s[2:3]
	global_load_dwordx4 v[36:39], v[26:27], off sc1 nt
	v_lshl_add_u64 v[26:27], v[26:27], 0, s[2:3]
	global_load_dwordx4 v[40:43], v[26:27], off sc1 nt
	v_lshl_add_u64 v[26:27], v[26:27], 0, s[2:3]
	global_load_dwordx4 v[44:47], v[26:27], off sc1 nt
	v_lshl_add_u64 v[26:27], v[26:27], 0, s[2:3]
	global_load_dwordx4 v[50:53], v[26:27], off sc1 nt
	v_lshl_add_u64 v[26:27], v[26:27], 0, s[2:3]
	global_load_dwordx4 v[54:57], v[26:27], off sc1 nt
	v_lshl_add_u64 v[26:27], v[26:27], 0, s[2:3]
	global_load_dwordx4 v[58:61], v[26:27], off sc1 nt
	s_nop 0
	global_load_dwordx4 v[24:27], v[24:25], off sc1 nt
	s_nop 0
	global_load_dwordx4 v[62:65], v[62:63], off sc1 nt
	v_ashrrev_i32_e32 v131, 31, v130
	s_and_b64 vcc, exec, s[10:11]
	s_cbranch_vccz .LBB0_402
	s_cmp_lt_u32 s0, 0x18000
	s_cbranch_scc0 .LBB0_403
	s_addk_i32 s1, 0xeaff
	s_lshr_b32 s12, s1, 10
	s_mov_b32 s13, 0
	s_lshl_b64 s[2:3], s[12:13], 22
	s_lshl_b64 s[10:11], s[12:13], 24
	s_add_u32 s1, s70, s10
	s_addc_u32 s14, s71, s11
	s_add_u32 s2, s90, s2
	s_addc_u32 s3, s91, s3
	s_add_u32 s10, s2, 0x3b100000
	s_addc_u32 s11, s3, 0
	s_lshl_b32 s2, s0, 1
	s_and_b32 s12, s2, 0x780
	s_lshl_b32 s2, s12, 13
	s_add_u32 s1, s1, s2
	s_addc_u32 s2, s14, 0
	s_lshl_b32 s3, s0, 5
	s_and_b32 s16, s3, 0x7e0
	s_lshl_b32 s3, s16, 2
	s_add_u32 s14, s1, s3
	s_mov_b32 s17, s13
	s_addc_u32 s15, s2, 0
	s_mov_b64 s[18:19], 0
	s_branch .LBB0_404

.LBB0_408:
	s_lshl_b64 s[0:1], s[8:9], 11
	s_add_u32 s0, s4, s0
	s_addc_u32 s1, s5, s1
	s_add_u32 s6, s0, s6
	s_addc_u32 s7, s1, s7
	s_lshl_b64 s[2:3], s[16:17], 11
	s_add_u32 s0, s10, s2
	s_addc_u32 s2, s11, s3
	s_add_u32 s4, s0, s12
	v_mov_b32_e32 v49, 0
	s_addc_u32 s5, s2, s13
	v_mad_i64_i32 v[68:69], s[2:3], s18, v130, 0
	v_lshl_add_u64 v[68:69], v[68:69], 2, s[14:15]
	v_mov_b32_e32 v67, v49
	s_mov_b32 s1, 0
	v_lshl_add_u64 v[66:67], v[68:69], 0, v[66:67]
	s_lshl_b32 s0, s18, 2
	v_lshl_add_u64 v[68:69], v[66:67], 0, s[0:1]
	v_lshl_add_u64 v[66:67], v[68:69], 0, s[0:1]
	v_lshl_add_u64 v[68:69], v[66:67], 0, s[0:1]
	v_lshl_add_u64 v[66:67], v[68:69], 0, s[0:1]
	v_lshl_add_u64 v[68:69], v[66:67], 0, s[0:1]
	v_lshl_add_u64 v[66:67], v[68:69], 0, s[0:1]
	v_lshl_add_u64 v[68:69], v[66:67], 0, s[0:1]
	v_lshl_add_u64 v[66:67], v[68:69], 0, s[0:1]
	v_lshl_add_u64 v[66:67], v[66:67], 0, s[0:1]
	v_lshl_add_u64 v[66:67], v[66:67], 0, s[0:1]
	v_lshl_add_u64 v[66:67], v[66:67], 0, s[0:1]
	v_lshl_add_u64 v[66:67], v[66:67], 0, s[0:1]
	v_lshl_add_u64 v[66:67], v[66:67], 0, s[0:1]
	v_lshl_add_u64 v[70:71], v[66:67], 0, s[0:1]
	v_lshl_add_u64 v[70:71], v[70:71], 0, s[0:1]
	s_waitcnt vmcnt(13)
	v_mul_f32_e32 v8, 0x44000000, v8
	v_mul_f32_e32 v4, 0x44000000, v4
	v_mov_b32_e32 v135, v49
	v_cvt_pk_fp8_f32 v135, v8, v4
	v_mul_f32_e32 v0, 0x44000000, v0
	s_waitcnt vmcnt(1)
	v_mul_f32_e32 v4, 0x44000000, v24
	v_mov_b32_e32 v136, v49
	v_cvt_pk_fp8_f32 v135, v0, v4 op_sel:[0,0,1]
	s_waitcnt vmcnt(0)
	v_mul_f32_e32 v0, 0x44000000, v63
	v_mul_f32_e32 v4, 0x44000000, v59
	v_cvt_pk_fp8_f32 v136, v0, v4
	v_mul_f32_e32 v0, 0x44000000, v45
	v_mul_f32_e32 v4, 0x44000000, v41
	v_mov_b32_e32 v137, v49
	v_cvt_pk_fp8_f32 v137, v0, v4
	v_mul_f32_e32 v28, 0x44000000, v28
	v_mul_f32_e32 v20, 0x44000000, v20
	v_mov_b32_e32 v134, v49
	v_mul_f32_e32 v0, 0x44000000, v37
	v_mul_f32_e32 v4, 0x44000000, v33
	v_mul_f32_e32 v62, 0x44000000, v62
	v_mul_f32_e32 v58, 0x44000000, v58
	v_mov_b32_e32 v132, v49
	v_mul_f32_e32 v44, 0x44000000, v44
	v_mul_f32_e32 v40, 0x44000000, v40
	v_mov_b32_e32 v133, v49
	v_cvt_pk_fp8_f32 v134, v28, v20
	v_cvt_pk_fp8_f32 v137, v0, v4 op_sel:[0,0,1]
	v_mul_f32_e32 v0, 0x44000000, v29
	v_mul_f32_e32 v4, 0x44000000, v21
	v_mov_b32_e32 v138, v49
	v_cvt_pk_fp8_f32 v132, v62, v58
	v_cvt_pk_fp8_f32 v133, v44, v40
	v_cvt_pk_fp8_f32 v138, v0, v4
	v_mul_f32_e32 v0, 0x44000000, v9
	v_mul_f32_e32 v4, 0x44000000, v5
	v_mov_b32_e32 v139, v49
	v_cvt_pk_fp8_f32 v139, v0, v4
	v_mul_f32_e32 v16, 0x44000000, v16
	v_mul_f32_e32 v12, 0x44000000, v12
	v_mul_f32_e32 v54, 0x44000000, v54
	v_mul_f32_e32 v50, 0x44000000, v50
	v_mul_f32_e32 v36, 0x44000000, v36
	v_mul_f32_e32 v32, 0x44000000, v32
	v_cvt_pk_fp8_f32 v134, v16, v12 op_sel:[0,0,1]
	v_mul_f32_e32 v8, 0x44000000, v55
	v_mul_f32_e32 v12, 0x44000000, v51
	v_cvt_pk_fp8_f32 v132, v54, v50 op_sel:[0,0,1]
	v_cvt_pk_fp8_f32 v133, v36, v32 op_sel:[0,0,1]
	v_cvt_pk_fp8_f32 v136, v8, v12 op_sel:[0,0,1]
	v_mul_f32_e32 v8, 0x44000000, v17
	v_mul_f32_e32 v12, 0x44000000, v13
	v_mul_f32_e32 v0, 0x44000000, v1
	v_mul_f32_e32 v1, 0x44000000, v25
	v_lshlrev_b32_e32 v48, 11, v48
	v_cvt_pk_fp8_f32 v138, v8, v12 op_sel:[0,0,1]
	v_cvt_pk_fp8_f32 v139, v0, v1 op_sel:[0,0,1]
	v_lshl_add_u64 v[0:1], s[6:7], 0, v[48:49]
	v_lshl_add_u64 v[0:1], v[0:1], 0, v[130:131]
	global_store_dwordx4 v[0:1], v[132:135], off sc1 nt
	global_store_dwordx4 v[0:1], v[136:139], off offset:2048 sc1 nt
	v_mul_f32_e32 v4, 0x44000000, v64
	v_mul_f32_e32 v5, 0x44000000, v60
	v_mov_b32_e32 v132, v49
	v_cvt_pk_fp8_f32 v132, v4, v5
	v_mul_f32_e32 v4, 0x44000000, v46
	v_mul_f32_e32 v5, 0x44000000, v42
	v_mov_b32_e32 v133, v49
	v_cvt_pk_fp8_f32 v133, v4, v5
	v_mul_f32_e32 v4, 0x44000000, v38
	v_mul_f32_e32 v5, 0x44000000, v34
	v_mov_b32_e32 v134, v49
	v_cvt_pk_fp8_f32 v133, v4, v5 op_sel:[0,0,1]
	v_mul_f32_e32 v4, 0x44000000, v30
	v_mul_f32_e32 v5, 0x44000000, v22
	v_cvt_pk_fp8_f32 v134, v4, v5
	v_mul_f32_e32 v4, 0x44000000, v10
	v_mul_f32_e32 v5, 0x44000000, v6
	v_mov_b32_e32 v135, v49
	v_cvt_pk_fp8_f32 v135, v4, v5
	v_mul_f32_e32 v8, 0x44000000, v56
	v_mul_f32_e32 v9, 0x44000000, v52
	v_mul_f32_e32 v2, 0x44000000, v2
	v_mul_f32_e32 v4, 0x44000000, v26
	v_cvt_pk_fp8_f32 v132, v8, v9 op_sel:[0,0,1]
	v_mul_f32_e32 v8, 0x44000000, v18
	v_mul_f32_e32 v9, 0x44000000, v14
	v_cvt_pk_fp8_f32 v135, v2, v4 op_sel:[0,0,1]
	v_mul_f32_e32 v2, 0x44000000, v65
	v_mul_f32_e32 v5, 0x44000000, v61
	v_mov_b32_e32 v4, v49
	v_cvt_pk_fp8_f32 v134, v8, v9 op_sel:[0,0,1]
	v_cvt_pk_fp8_f32 v4, v2, v5
	v_mul_f32_e32 v2, 0x44000000, v47
	v_mul_f32_e32 v9, 0x44000000, v43
	v_mov_b32_e32 v5, v49
	v_cvt_pk_fp8_f32 v5, v2, v9
	v_mul_f32_e32 v6, 0x44000000, v57
	v_mul_f32_e32 v8, 0x44000000, v53
	v_cvt_pk_fp8_f32 v4, v6, v8 op_sel:[0,0,1]
	v_mul_f32_e32 v2, 0x44000000, v39
	v_mul_f32_e32 v6, 0x44000000, v35
	v_cvt_pk_fp8_f32 v5, v2, v6 op_sel:[0,0,1]
	v_mul_f32_e32 v2, 0x44000000, v31
	v_mul_f32_e32 v8, 0x44000000, v23
	v_mov_b32_e32 v6, v49
	v_cvt_pk_fp8_f32 v6, v2, v8
	v_mul_f32_e32 v2, 0x44000000, v11
	v_mul_f32_e32 v8, 0x44000000, v7
	v_mov_b32_e32 v7, v49
	v_cvt_pk_fp8_f32 v7, v2, v8
	v_mul_f32_e32 v9, 0x44000000, v19
	v_mul_f32_e32 v10, 0x44000000, v15
	v_mul_f32_e32 v2, 0x44000000, v3
	v_mul_f32_e32 v3, 0x44000000, v27
	s_movk_i32 s0, 0x1000
	v_cvt_pk_fp8_f32 v6, v9, v10 op_sel:[0,0,1]
	v_cvt_pk_fp8_f32 v7, v2, v3 op_sel:[0,0,1]
	v_add_co_u32_e32 v0, vcc, s0, v0
	s_waitcnt vmcnt(16)
	v_mul_f32_e32 v2, 0x44000000, v86
	v_addc_co_u32_e32 v1, vcc, 0, v1, vcc
	global_store_dwordx4 v[0:1], v[132:135], off sc1 nt
	global_store_dwordx4 v[0:1], v[4:7], off offset:2048 sc1 nt
	s_branch .Lside_done_2
	v_mul_f32_e32 v1, 0x44000000, v82
	v_mov_b32_e32 v0, v49
	v_cvt_pk_fp8_f32 v0, v1, v2
	s_waitcnt vmcnt(15)
	v_mul_f32_e32 v2, 0x44000000, v110
	s_waitcnt vmcnt(14)
	v_mul_f32_e32 v5, 0x44000000, v114
	v_mov_b32_e32 v1, v49
	v_cvt_pk_fp8_f32 v1, v2, v5
	v_mul_f32_e32 v3, 0x44000000, v122
	v_mul_f32_e32 v4, 0x44000000, v126
	v_cvt_pk_fp8_f32 v0, v3, v4 op_sel:[0,0,1]
	s_waitcnt vmcnt(13)
	v_mul_f32_e32 v2, 0x44000000, v90
	s_waitcnt vmcnt(12)
	v_mul_f32_e32 v3, 0x44000000, v94
	v_cvt_pk_fp8_f32 v1, v2, v3 op_sel:[0,0,1]
	s_waitcnt vmcnt(11)
	v_mul_f32_e32 v3, 0x44000000, v74
	s_waitcnt vmcnt(10)
	v_mul_f32_e32 v4, 0x44000000, v98
	v_mov_b32_e32 v2, v49
	v_cvt_pk_fp8_f32 v2, v3, v4
	s_waitcnt vmcnt(7)
	v_mul_f32_e32 v4, 0x44000000, v78
	s_waitcnt vmcnt(6)
	v_mul_f32_e32 v7, 0x44000000, v102
	v_mov_b32_e32 v3, v49
	v_cvt_pk_fp8_f32 v3, v4, v7
	v_mul_f32_e32 v5, 0x44000000, v106
	v_mul_f32_e32 v6, 0x44000000, v118
	v_cvt_pk_fp8_f32 v2, v5, v6 op_sel:[0,0,1]
	s_waitcnt vmcnt(5)
	v_mul_f32_e32 v4, 0x44000000, v66
	s_waitcnt vmcnt(4)
	v_mul_f32_e32 v5, 0x44000000, v70
	v_cvt_pk_fp8_f32 v3, v4, v5 op_sel:[0,0,1]
	v_mul_f32_e32 v5, 0x44000000, v83
	v_mul_f32_e32 v6, 0x44000000, v87
	v_mov_b32_e32 v4, v49
	v_cvt_pk_fp8_f32 v4, v5, v6
	v_mul_f32_e32 v6, 0x44000000, v111
	v_mul_f32_e32 v9, 0x44000000, v115
	v_mov_b32_e32 v5, v49
	v_cvt_pk_fp8_f32 v5, v6, v9
	v_mul_f32_e32 v7, 0x44000000, v123
	v_mul_f32_e32 v8, 0x44000000, v127
	v_cvt_pk_fp8_f32 v4, v7, v8 op_sel:[0,0,1]
	v_mul_f32_e32 v6, 0x44000000, v91
	v_mul_f32_e32 v7, 0x44000000, v95
	v_cvt_pk_fp8_f32 v5, v6, v7 op_sel:[0,0,1]
	v_mul_f32_e32 v7, 0x44000000, v75
	v_mul_f32_e32 v8, 0x44000000, v99
	v_mov_b32_e32 v6, v49
	v_cvt_pk_fp8_f32 v6, v7, v8
	v_mul_f32_e32 v8, 0x44000000, v79
	v_mul_f32_e32 v11, 0x44000000, v103
	v_mov_b32_e32 v7, v49
	v_cvt_pk_fp8_f32 v7, v8, v11
	v_mul_f32_e32 v9, 0x44000000, v107
	v_mul_f32_e32 v10, 0x44000000, v119
	v_cvt_pk_fp8_f32 v6, v9, v10 op_sel:[0,0,1]
	v_mul_f32_e32 v8, 0x44000000, v67
	v_mul_f32_e32 v9, 0x44000000, v71
	v_cvt_pk_fp8_f32 v7, v8, v9 op_sel:[0,0,1]
	v_lshl_add_u64 v[8:9], s[4:5], 0, v[48:49]
	v_lshl_add_u64 v[8:9], v[8:9], 0, v[130:131]
	global_store_dwordx4 v[8:9], v[0:3], off sc1 nt
	global_store_dwordx4 v[8:9], v[4:7], off offset:2048 sc1 nt
	v_mov_b32_e32 v46, v49
	v_mul_f32_e32 v1, 0x44000000, v84
	v_mul_f32_e32 v2, 0x44000000, v88
	v_mov_b32_e32 v0, v49
	v_cvt_pk_fp8_f32 v0, v1, v2
	v_mul_f32_e32 v2, 0x44000000, v112
	v_mul_f32_e32 v5, 0x44000000, v116
	v_mov_b32_e32 v1, v49
	v_cvt_pk_fp8_f32 v1, v2, v5
	v_mul_f32_e32 v3, 0x44000000, v124
	v_mul_f32_e32 v4, 0x44000000, v128
	v_cvt_pk_fp8_f32 v0, v3, v4 op_sel:[0,0,1]
	v_mul_f32_e32 v2, 0x44000000, v92
	v_mul_f32_e32 v3, 0x44000000, v96
	v_cvt_pk_fp8_f32 v1, v2, v3 op_sel:[0,0,1]
	v_mul_f32_e32 v3, 0x44000000, v76
	v_mul_f32_e32 v4, 0x44000000, v100
	v_mov_b32_e32 v2, v49
	v_cvt_pk_fp8_f32 v2, v3, v4
	v_mul_f32_e32 v4, 0x44000000, v80
	v_mul_f32_e32 v7, 0x44000000, v104
	v_mov_b32_e32 v3, v49
	v_cvt_pk_fp8_f32 v3, v4, v7
	v_mul_f32_e32 v5, 0x44000000, v108
	v_mul_f32_e32 v6, 0x44000000, v120
	v_cvt_pk_fp8_f32 v2, v5, v6 op_sel:[0,0,1]
	v_mul_f32_e32 v4, 0x44000000, v68
	v_mul_f32_e32 v5, 0x44000000, v72
	v_cvt_pk_fp8_f32 v3, v4, v5 op_sel:[0,0,1]
	v_mul_f32_e32 v4, 0x44000000, v85
	v_mul_f32_e32 v5, 0x44000000, v89
	v_cvt_pk_fp8_f32 v46, v4, v5
	v_mul_f32_e32 v4, 0x44000000, v113
	v_mul_f32_e32 v5, 0x44000000, v117
	v_mov_b32_e32 v47, v49
	v_cvt_pk_fp8_f32 v47, v4, v5
	v_mul_f32_e32 v4, 0x44000000, v93
	v_mul_f32_e32 v5, 0x44000000, v97
	v_mov_b32_e32 v48, v49
	v_cvt_pk_fp8_f32 v47, v4, v5 op_sel:[0,0,1]
	v_mul_f32_e32 v4, 0x44000000, v77
	v_mul_f32_e32 v5, 0x44000000, v101
	v_cvt_pk_fp8_f32 v48, v4, v5
	v_mul_f32_e32 v4, 0x44000000, v81
	v_mul_f32_e32 v5, 0x44000000, v105
	v_cvt_pk_fp8_f32 v49, v4, v5
	v_mul_f32_e32 v6, 0x44000000, v125
	v_mul_f32_e32 v7, 0x44000000, v129
	v_cvt_pk_fp8_f32 v46, v6, v7 op_sel:[0,0,1]
	v_mul_f32_e32 v6, 0x44000000, v109
	v_mul_f32_e32 v7, 0x44000000, v121
	v_mul_f32_e32 v4, 0x44000000, v69
	v_mul_f32_e32 v5, 0x44000000, v73
	v_cvt_pk_fp8_f32 v48, v6, v7 op_sel:[0,0,1]
	v_cvt_pk_fp8_f32 v49, v4, v5 op_sel:[0,0,1]
	v_add_co_u32_e32 v4, vcc, s0, v8
	s_nop 1
	v_addc_co_u32_e32 v5, vcc, 0, v9, vcc
	global_store_dwordx4 v[4:5], v[0:3], off sc1 nt
	global_store_dwordx4 v[4:5], v[46:49], off offset:2048 sc1 nt
.Lside_done_2:
	s_waitcnt vmcnt(0)
.LBB0_409:
	s_mov_b64 s[4:5], 0

.LBB0_558:
	s_cmp_gt_i32 s95, 5
	s_cselect_b64 s[6:7], -1, 0
	s_and_b64 s[0:1], s[52:53], s[6:7]
	s_andn2_b64 vcc, exec, s[0:1]
	s_cbranch_vccnz .LBB0_636
	s_waitcnt vmcnt(0)
	v_readlane_b32 s0, v255, 0
	s_cmp_gt_u32 s0, 63
	s_mov_b64 s[4:5], -1
	s_barrier
	s_cbranch_scc0 .LBB0_581
	v_readlane_b32 s0, v255, 0
	s_cmpk_gt_u32 s0, 0x1ff
	s_cbranch_scc1 .LBB0_580
	v_readlane_b32 s0, v255, 4
	s_mul_i32 s1, s0, 7
	v_readlane_b32 s0, v255, 28
	s_add_i32 s1, s1, s0
	s_add_i32 s0, s1, 0xf1ff
	s_cmp_gt_i32 s0, 0xffff
	s_cselect_b64 s[12:13], -1, 0
	s_and_b64 vcc, exec, s[12:13]
	s_waitcnt vmcnt(5)
	v_mbcnt_lo_u32_b32 v0, -1, 0
	v_mbcnt_hi_u32_b32 v0, -1, v0
	s_cbranch_vccz .LBB0_564
	s_cmp_lt_u32 s0, 0x18000
	s_cbranch_scc0 .LBB0_565
	s_add_i32 s2, s1, 0xfffff1ff
	s_lshr_b32 s8, s2, 10
	s_mov_b32 s9, 0
	s_lshl_b64 s[2:3], s[8:9], 22
	s_lshl_b64 s[4:5], s[8:9], 24
	s_add_u32 s10, s70, s4
	s_addc_u32 s11, s71, s5
	s_add_u32 s2, s90, s2
	s_addc_u32 s3, s91, s3
	s_add_u32 s4, s2, 0x3b100000
	s_addc_u32 s5, s3, 0
	s_lshl_b32 s2, s0, 1
	s_and_b32 s8, s2, 0x780
	s_lshl_b32 s2, s8, 13
	s_add_u32 s2, s10, s2
	s_addc_u32 s3, s11, 0
	s_lshl_b32 s10, s0, 5
	s_and_b32 s10, s10, 0x7e0
	s_lshl_b32 s14, s10, 2
	s_add_u32 s14, s2, s14
	s_mov_b32 s11, s9
	s_addc_u32 s15, s3, 0
	s_mov_b64 s[16:17], 0
	s_branch .LBB0_566

.LBB0_570:
	v_lshlrev_b32_e32 v1, 1, v0
	v_and_b32_e32 v130, -16, v1
	v_lshlrev_b32_e32 v0, 2, v0
	v_and_b32_e32 v48, 28, v0
	v_mad_i64_i32 v[0:1], s[18:19], s16, v130, 0
	v_mov_b32_e32 v67, 0
	v_lshl_add_u64 v[0:1], v[0:1], 2, s[14:15]
	v_lshlrev_b32_e32 v66, 2, v48
	s_mov_b32 s3, 0
	v_lshl_add_u64 v[62:63], v[0:1], 0, v[66:67]
	s_mul_i32 s2, s16, 60
	v_lshl_add_u64 v[24:25], v[62:63], 0, s[2:3]
	s_lshl_b32 s2, s16, 2
	s_sub_u32 s2, 0, s2
	s_subb_u32 s3, 0, 0
	v_lshl_add_u64 v[0:1], v[24:25], 0, s[2:3]
	v_lshl_add_u64 v[8:9], v[0:1], 0, s[2:3]
	global_load_dwordx4 v[0:3], v[0:1], off sc1 nt
	s_nop 0
	global_load_dwordx4 v[4:7], v[8:9], off sc1 nt
	v_lshl_add_u64 v[8:9], v[8:9], 0, s[2:3]
	v_lshl_add_u64 v[16:17], v[8:9], 0, s[2:3]
	global_load_dwordx4 v[8:11], v[8:9], off sc1 nt
	s_nop 0
	global_load_dwordx4 v[12:15], v[16:17], off sc1 nt
	v_lshl_add_u64 v[16:17], v[16:17], 0, s[2:3]
	v_lshl_add_u64 v[26:27], v[16:17], 0, s[2:3]
	global_load_dwordx4 v[16:19], v[16:17], off sc1 nt
	s_nop 0
	global_load_dwordx4 v[20:23], v[26:27], off sc1 nt
	v_lshl_add_u64 v[26:27], v[26:27], 0, s[2:3]
	global_load_dwordx4 v[28:31], v[26:27], off sc1 nt
	v_lshl_add_u64 v[26:27], v[26:27], 0, s[2:3]
	global_load_dwordx4 v[32:35], v[26:27], off sc1 nt
	v_lshl_add_u64 v[26:27], v[26:27], 0, s[2:3]
	global_load_dwordx4 v[36:39], v[26:27], off sc1 nt
	v_lshl_add_u64 v[26:27], v[26:27], 0, s[2:3]
	global_load_dwordx4 v[40:43], v[26:27], off sc1 nt
	v_lshl_add_u64 v[26:27], v[26:27], 0, s[2:3]
	global_load_dwordx4 v[44:47], v[26:27], off sc1 nt
	v_lshl_add_u64 v[26:27], v[26:27], 0, s[2:3]
	global_load_dwordx4 v[50:53], v[26:27], off sc1 nt
	v_lshl_add_u64 v[26:27], v[26:27], 0, s[2:3]
	global_load_dwordx4 v[54:57], v[26:27], off sc1 nt
	v_lshl_add_u64 v[26:27], v[26:27], 0, s[2:3]
	global_load_dwordx4 v[58:61], v[26:27], off sc1 nt
	s_nop 0
	global_load_dwordx4 v[24:27], v[24:25], off sc1 nt
	s_nop 0
	global_load_dwordx4 v[62:65], v[62:63], off sc1 nt
	v_ashrrev_i32_e32 v131, 31, v130
	s_and_b64 vcc, exec, s[12:13]
	s_cbranch_vccz .LBB0_573
	s_cmp_lt_u32 s0, 0x18000
	s_cbranch_scc0 .LBB0_574
	s_addk_i32 s1, 0xf1ff
	s_lshr_b32 s14, s1, 10
	s_mov_b32 s15, 0
	s_lshl_b64 s[2:3], s[14:15], 22
	s_lshl_b64 s[12:13], s[14:15], 24
	s_add_u32 s1, s70, s12
	s_addc_u32 s16, s71, s13
	s_add_u32 s2, s90, s2
	s_addc_u32 s3, s91, s3
	s_add_u32 s12, s2, 0x3b100000
	s_addc_u32 s13, s3, 0
	s_lshl_b32 s2, s0, 1
	s_and_b32 s14, s2, 0x780
	s_lshl_b32 s2, s14, 13
	s_add_u32 s1, s1, s2
	s_addc_u32 s2, s16, 0
	s_lshl_b32 s3, s0, 5
	s_and_b32 s18, s3, 0x7e0
	s_lshl_b32 s3, s18, 2
	s_add_u32 s16, s1, s3
	s_mov_b32 s19, s15
	s_addc_u32 s17, s2, 0
	s_mov_b64 s[20:21], 0
	s_branch .LBB0_575

.Lside_done_3:
	s_waitcnt vmcnt(0)
.LBB0_580:
	s_mov_b64 s[4:5], 0

.LBB0_645:
	v_readlane_b32 s0, v255, 4
	s_and_b64 vcc, exec, s[36:37]
	s_mul_i32 s38, s0, 13
	s_cbranch_vccnz .LBB0_676
	v_readlane_b32 s0, v255, 28
	s_add_i32 s0, s0, s38
	s_add_i32 s1, s38, 0xd00d
	s_add_i32 s0, s0, 0xd000
	s_cmp_ge_i32 s0, s1
	s_cbranch_scc1 .LBB0_676
	s_cmp_gt_i32 s0, 0xffff
	s_waitcnt vmcnt(5)
	v_mbcnt_lo_u32_b32 v0, -1, 0
	v_mbcnt_hi_u32_b32 v0, -1, v0
	s_cbranch_scc0 .LBB0_650
	s_cmp_lt_u32 s0, 0x18000
	s_cbranch_scc0 .LBB0_651
	s_add_i32 s2, s0, 0xffff0000
	s_lshr_b32 s14, s2, 10
	s_mov_b32 s15, 0
	s_lshl_b64 s[2:3], s[14:15], 22
	s_lshl_b64 s[6:7], s[14:15], 24
	s_add_u32 s6, s70, s6
	s_addc_u32 s7, s71, s7
	s_add_u32 s2, s90, s2
	s_addc_u32 s3, s91, s3
	s_add_u32 s12, s2, 0x3b100000
	s_addc_u32 s13, s3, 0
	s_lshl_b32 s2, s0, 1
	s_and_b32 s14, s2, 0x780
	s_lshl_b32 s2, s14, 13
	s_add_u32 s2, s6, s2
	s_addc_u32 s3, s7, 0
	s_lshl_b32 s6, s0, 5
	s_and_b32 s16, s6, 0x7e0
	s_lshl_b32 s6, s16, 2
	s_add_u32 s18, s2, s6
	s_mov_b32 s17, s15
	s_addc_u32 s19, s3, 0
	s_mov_b64 s[6:7], 0
	s_branch .LBB0_652

.LBB0_737:
	s_andn2_b64 vcc, exec, s[36:37]
	s_cbranch_vccnz .LBB0_768
	v_readlane_b32 s0, v255, 28
	s_add_i32 s0, s0, s38
	s_add_i32 s1, s38, 0xd00d
	s_add_i32 s0, s0, 0xd000
	s_cmp_ge_i32 s0, s1
	s_cbranch_scc1 .LBB0_768
	s_cmp_gt_i32 s0, 0xffff
	v_mbcnt_lo_u32_b32 v0, -1, 0
	v_mbcnt_hi_u32_b32 v0, -1, v0
	s_cbranch_scc0 .LBB0_742
	s_cmp_lt_u32 s0, 0x18000
	s_cbranch_scc0 .LBB0_743
	s_add_i32 s2, s0, 0xffff0000
	s_lshr_b32 s10, s2, 10
	s_mov_b32 s11, 0
	s_lshl_b64 s[2:3], s[10:11], 22
	s_lshl_b64 s[4:5], s[10:11], 24
	s_add_u32 s4, s70, s4
	s_addc_u32 s5, s71, s5
	s_add_u32 s2, s90, s2
	s_addc_u32 s3, s91, s3
	s_add_u32 s6, s2, 0x3b100000
	s_addc_u32 s7, s3, 0
	s_lshl_b32 s2, s0, 1
	s_and_b32 s10, s2, 0x780
	s_lshl_b32 s2, s10, 13
	s_add_u32 s2, s4, s2
	s_addc_u32 s3, s5, 0
	s_lshl_b32 s4, s0, 5
	s_and_b32 s12, s4, 0x7e0
	s_lshl_b32 s4, s12, 2
	s_add_u32 s14, s2, s4
	s_mov_b32 s13, s11
	s_addc_u32 s15, s3, 0
	s_mov_b64 s[4:5], 0
	s_branch .LBB0_744

.LBB0_768:
	s_cmp_gt_i32 s95, 6
	s_cselect_b64 s[4:5], -1, 0
	s_and_b64 s[0:1], s[8:9], s[4:5]
	s_andn2_b64 vcc, exec, s[0:1]
	s_cbranch_vccnz .LBB0_846
	s_waitcnt vmcnt(0)
	v_readlane_b32 s0, v255, 0
	s_cmp_gt_u32 s0, 63
	s_mov_b64 s[6:7], -1
	s_waitcnt vmcnt(63) expcnt(7) lgkmcnt(15)
	s_barrier
	s_cbranch_scc0 .LBB0_791
	v_readlane_b32 s0, v255, 0
	s_cmpk_gt_u32 s0, 0x1ff
	s_cbranch_scc1 .LBB0_790
	v_readlane_b32 s0, v255, 4
	s_mul_i32 s1, s0, 7
	v_readlane_b32 s0, v255, 28
	s_add_i32 s1, s1, s0
	s_add_i32 s0, s1, 0xf8ff
	s_cmp_gt_i32 s0, 0xffff
	s_cselect_b64 s[12:13], -1, 0
	s_and_b64 vcc, exec, s[12:13]
	s_waitcnt vmcnt(5)
	v_mbcnt_lo_u32_b32 v0, -1, 0
	v_mbcnt_hi_u32_b32 v0, -1, v0
	s_cbranch_vccz .LBB0_774
	s_cmp_lt_u32 s0, 0x18000
	s_cbranch_scc0 .LBB0_775
	s_add_i32 s2, s1, 0xfffff8ff
	s_lshr_b32 s8, s2, 10
	s_mov_b32 s9, 0
	s_lshl_b64 s[2:3], s[8:9], 22
	s_lshl_b64 s[6:7], s[8:9], 24
	s_add_u32 s10, s70, s6
	s_addc_u32 s11, s71, s7
	s_add_u32 s2, s90, s2
	s_addc_u32 s3, s91, s3
	s_add_u32 s6, s2, 0x3b100000
	s_addc_u32 s7, s3, 0
	s_lshl_b32 s2, s0, 1
	s_and_b32 s8, s2, 0x780
	s_lshl_b32 s2, s8, 13
	s_add_u32 s2, s10, s2
	s_addc_u32 s3, s11, 0
	s_lshl_b32 s10, s0, 5
	s_and_b32 s10, s10, 0x7e0
	s_lshl_b32 s14, s10, 2
	s_add_u32 s14, s2, s14
	s_mov_b32 s11, s9
	s_addc_u32 s15, s3, 0
	s_mov_b64 s[16:17], 0
	s_branch .LBB0_776

.LBB0_780:
	v_lshlrev_b32_e32 v1, 1, v0
	v_and_b32_e32 v130, -16, v1
	v_lshlrev_b32_e32 v0, 2, v0
	v_and_b32_e32 v48, 28, v0
	v_mad_i64_i32 v[0:1], s[18:19], s16, v130, 0
	v_mov_b32_e32 v67, 0
	v_lshl_add_u64 v[0:1], v[0:1], 2, s[14:15]
	v_lshlrev_b32_e32 v66, 2, v48
	s_mov_b32 s3, 0
	v_lshl_add_u64 v[62:63], v[0:1], 0, v[66:67]
	s_mul_i32 s2, s16, 60
	v_lshl_add_u64 v[24:25], v[62:63], 0, s[2:3]
	s_lshl_b32 s2, s16, 2
	s_sub_u32 s2, 0, s2
	s_subb_u32 s3, 0, 0
	v_lshl_add_u64 v[0:1], v[24:25], 0, s[2:3]
	v_lshl_add_u64 v[8:9], v[0:1], 0, s[2:3]
	global_load_dwordx4 v[0:3], v[0:1], off sc1 nt
	s_nop 0
	global_load_dwordx4 v[4:7], v[8:9], off sc1 nt
	v_lshl_add_u64 v[8:9], v[8:9], 0, s[2:3]
	v_lshl_add_u64 v[16:17], v[8:9], 0, s[2:3]
	global_load_dwordx4 v[8:11], v[8:9], off sc1 nt
	s_nop 0
	global_load_dwordx4 v[12:15], v[16:17], off sc1 nt
	v_lshl_add_u64 v[16:17], v[16:17], 0, s[2:3]
	v_lshl_add_u64 v[26:27], v[16:17], 0, s[2:3]
	global_load_dwordx4 v[16:19], v[16:17], off sc1 nt
	s_nop 0
	global_load_dwordx4 v[20:23], v[26:27], off sc1 nt
	v_lshl_add_u64 v[26:27], v[26:27], 0, s[2:3]
	global_load_dwordx4 v[28:31], v[26:27], off sc1 nt
	v_lshl_add_u64 v[26:27], v[26:27], 0, s[2:3]
	global_load_dwordx4 v[32:35], v[26:27], off sc1 nt
	v_lshl_add_u64 v[26:27], v[26:27], 0, s[2:3]
	global_load_dwordx4 v[36:39], v[26:27], off sc1 nt
	v_lshl_add_u64 v[26:27], v[26:27], 0, s[2:3]
	global_load_dwordx4 v[40:43], v[26:27], off sc1 nt
	v_lshl_add_u64 v[26:27], v[26:27], 0, s[2:3]
	global_load_dwordx4 v[44:47], v[26:27], off sc1 nt
	v_lshl_add_u64 v[26:27], v[26:27], 0, s[2:3]
	global_load_dwordx4 v[50:53], v[26:27], off sc1 nt
	v_lshl_add_u64 v[26:27], v[26:27], 0, s[2:3]
	global_load_dwordx4 v[54:57], v[26:27], off sc1 nt
	v_lshl_add_u64 v[26:27], v[26:27], 0, s[2:3]
	global_load_dwordx4 v[58:61], v[26:27], off sc1 nt
	s_nop 0
	global_load_dwordx4 v[24:27], v[24:25], off sc1 nt
	s_nop 0
	global_load_dwordx4 v[62:65], v[62:63], off sc1 nt
	v_ashrrev_i32_e32 v131, 31, v130
	s_and_b64 vcc, exec, s[12:13]
	s_cbranch_vccz .LBB0_783
	s_cmp_lt_u32 s0, 0x18000
	s_cbranch_scc0 .LBB0_784
	s_addk_i32 s1, 0xf8ff
	s_lshr_b32 s14, s1, 10
	s_mov_b32 s15, 0
	s_lshl_b64 s[2:3], s[14:15], 22
	s_lshl_b64 s[12:13], s[14:15], 24
	s_add_u32 s1, s70, s12
	s_addc_u32 s16, s71, s13
	s_add_u32 s2, s90, s2
	s_addc_u32 s3, s91, s3
	s_add_u32 s12, s2, 0x3b100000
	s_addc_u32 s13, s3, 0
	s_lshl_b32 s2, s0, 1
	s_and_b32 s14, s2, 0x780
	s_lshl_b32 s2, s14, 13
	s_add_u32 s1, s1, s2
	s_addc_u32 s2, s16, 0
	s_lshl_b32 s3, s0, 5
	s_and_b32 s18, s3, 0x7e0
	s_lshl_b32 s3, s18, 2
	s_add_u32 s16, s1, s3
	s_mov_b32 s19, s15
	s_addc_u32 s17, s2, 0
	s_mov_b64 s[20:21], 0
	s_branch .LBB0_785

.Lside_done_4:
	s_waitcnt vmcnt(0)
.LBB0_790:
	s_mov_b64 s[6:7], 0

.LBB0_900:
	s_cmp_gt_i32 s95, 7
	s_cselect_b64 s[6:7], -1, 0
	s_and_b64 s[0:1], s[4:5], s[6:7]
	s_andn2_b64 vcc, exec, s[0:1]
	s_cbranch_vccnz .LBB0_978
	s_waitcnt vmcnt(0)
	v_readlane_b32 s0, v255, 0
	s_cmp_gt_u32 s0, 63
	s_mov_b64 s[4:5], -1
	s_waitcnt vmcnt(63) expcnt(7) lgkmcnt(15)
	s_barrier
	s_cbranch_scc0 .LBB0_923
	v_readlane_b32 s0, v255, 0
	s_cmpk_gt_u32 s0, 0x1ff
	s_cbranch_scc1 .LBB0_922
	v_readlane_b32 s0, v255, 4
	s_mul_i32 s1, s0, 7
	v_readlane_b32 s0, v255, 28
	s_add_i32 s1, s1, s0
	s_add_i32 s0, s1, 0x178ff
	s_cmp_gt_i32 s0, 0xffff
	s_cselect_b64 s[12:13], -1, 0
	s_and_b64 vcc, exec, s[12:13]
	s_waitcnt vmcnt(5)
	v_mbcnt_lo_u32_b32 v0, -1, 0
	v_mbcnt_hi_u32_b32 v0, -1, v0
	s_cbranch_vccz .LBB0_906
	s_cmp_lt_u32 s0, 0x18000
	s_cbranch_scc0 .LBB0_907
	s_add_i32 s2, s1, 0x78ff
	s_lshr_b32 s8, s2, 10
	s_mov_b32 s9, 0
	s_lshl_b64 s[2:3], s[8:9], 22
	s_lshl_b64 s[4:5], s[8:9], 24
	s_add_u32 s10, s70, s4
	s_addc_u32 s11, s71, s5
	s_add_u32 s2, s90, s2
	s_addc_u32 s3, s91, s3
	s_add_u32 s4, s2, 0x3b100000
	s_addc_u32 s5, s3, 0
	s_lshl_b32 s2, s0, 1
	s_and_b32 s8, s2, 0x780
	s_lshl_b32 s2, s8, 13
	s_add_u32 s2, s10, s2
	s_addc_u32 s3, s11, 0
	s_lshl_b32 s10, s0, 5
	s_and_b32 s10, s10, 0x7e0
	s_lshl_b32 s14, s10, 2
	s_add_u32 s14, s2, s14
	s_mov_b32 s11, s9
	s_addc_u32 s15, s3, 0
	s_mov_b64 s[16:17], 0
	s_branch .LBB0_908

.LBB0_912:
	v_lshlrev_b32_e32 v1, 1, v0
	v_and_b32_e32 v130, -16, v1
	v_lshlrev_b32_e32 v0, 2, v0
	v_and_b32_e32 v48, 28, v0
	v_mad_i64_i32 v[0:1], s[18:19], s16, v130, 0
	v_mov_b32_e32 v67, 0
	v_lshl_add_u64 v[0:1], v[0:1], 2, s[14:15]
	v_lshlrev_b32_e32 v66, 2, v48
	s_mov_b32 s3, 0
	v_lshl_add_u64 v[62:63], v[0:1], 0, v[66:67]
	s_mul_i32 s2, s16, 60
	v_lshl_add_u64 v[24:25], v[62:63], 0, s[2:3]
	s_lshl_b32 s2, s16, 2
	s_sub_u32 s2, 0, s2
	s_subb_u32 s3, 0, 0
	v_lshl_add_u64 v[0:1], v[24:25], 0, s[2:3]
	v_lshl_add_u64 v[8:9], v[0:1], 0, s[2:3]
	global_load_dwordx4 v[0:3], v[0:1], off sc1 nt
	s_nop 0
	global_load_dwordx4 v[4:7], v[8:9], off sc1 nt
	v_lshl_add_u64 v[8:9], v[8:9], 0, s[2:3]
	v_lshl_add_u64 v[16:17], v[8:9], 0, s[2:3]
	global_load_dwordx4 v[8:11], v[8:9], off sc1 nt
	s_nop 0
	global_load_dwordx4 v[12:15], v[16:17], off sc1 nt
	v_lshl_add_u64 v[16:17], v[16:17], 0, s[2:3]
	v_lshl_add_u64 v[26:27], v[16:17], 0, s[2:3]
	global_load_dwordx4 v[16:19], v[16:17], off sc1 nt
	s_nop 0
	global_load_dwordx4 v[20:23], v[26:27], off sc1 nt
	v_lshl_add_u64 v[26:27], v[26:27], 0, s[2:3]
	global_load_dwordx4 v[28:31], v[26:27], off sc1 nt
	v_lshl_add_u64 v[26:27], v[26:27], 0, s[2:3]
	global_load_dwordx4 v[32:35], v[26:27], off sc1 nt
	v_lshl_add_u64 v[26:27], v[26:27], 0, s[2:3]
	global_load_dwordx4 v[36:39], v[26:27], off sc1 nt
	v_lshl_add_u64 v[26:27], v[26:27], 0, s[2:3]
	global_load_dwordx4 v[40:43], v[26:27], off sc1 nt
	v_lshl_add_u64 v[26:27], v[26:27], 0, s[2:3]
	global_load_dwordx4 v[44:47], v[26:27], off sc1 nt
	v_lshl_add_u64 v[26:27], v[26:27], 0, s[2:3]
	global_load_dwordx4 v[50:53], v[26:27], off sc1 nt
	v_lshl_add_u64 v[26:27], v[26:27], 0, s[2:3]
	global_load_dwordx4 v[54:57], v[26:27], off sc1 nt
	v_lshl_add_u64 v[26:27], v[26:27], 0, s[2:3]
	global_load_dwordx4 v[58:61], v[26:27], off sc1 nt
	s_nop 0
	global_load_dwordx4 v[24:27], v[24:25], off sc1 nt
	s_nop 0
	global_load_dwordx4 v[62:65], v[62:63], off sc1 nt
	v_ashrrev_i32_e32 v131, 31, v130
	s_and_b64 vcc, exec, s[12:13]
	s_cbranch_vccz .LBB0_915
	s_cmp_lt_u32 s0, 0x18000
	s_cbranch_scc0 .LBB0_916
	s_addk_i32 s1, 0x78ff
	s_lshr_b32 s14, s1, 10
	s_mov_b32 s15, 0
	s_lshl_b64 s[2:3], s[14:15], 22
	s_lshl_b64 s[12:13], s[14:15], 24
	s_add_u32 s1, s70, s12
	s_addc_u32 s16, s71, s13
	s_add_u32 s2, s90, s2
	s_addc_u32 s3, s91, s3
	s_add_u32 s12, s2, 0x3b100000
	s_addc_u32 s13, s3, 0
	s_lshl_b32 s2, s0, 1
	s_and_b32 s14, s2, 0x780
	s_lshl_b32 s2, s14, 13
	s_add_u32 s1, s1, s2
	s_addc_u32 s2, s16, 0
	s_lshl_b32 s3, s0, 5
	s_and_b32 s18, s3, 0x7e0
	s_lshl_b32 s3, s18, 2
	s_add_u32 s16, s1, s3
	s_mov_b32 s19, s15
	s_addc_u32 s17, s2, 0
	s_mov_b64 s[20:21], 0
	s_branch .LBB0_917

.LBB0_921:
	s_lshl_b64 s[0:1], s[10:11], 11
	s_add_u32 s0, s4, s0
	s_addc_u32 s1, s5, s1
	s_add_u32 s8, s0, s8
	s_addc_u32 s9, s1, s9
	s_lshl_b64 s[2:3], s[18:19], 11
	s_add_u32 s0, s12, s2
	s_addc_u32 s2, s13, s3
	s_add_u32 s4, s0, s14
	v_mov_b32_e32 v49, 0
	s_addc_u32 s5, s2, s15
	v_mad_i64_i32 v[68:69], s[2:3], s20, v130, 0
	v_lshl_add_u64 v[68:69], v[68:69], 2, s[16:17]
	v_mov_b32_e32 v67, v49
	s_mov_b32 s1, 0
	v_lshl_add_u64 v[66:67], v[68:69], 0, v[66:67]
	s_lshl_b32 s0, s20, 2
	v_lshl_add_u64 v[68:69], v[66:67], 0, s[0:1]
	v_lshl_add_u64 v[66:67], v[68:69], 0, s[0:1]
	v_lshl_add_u64 v[68:69], v[66:67], 0, s[0:1]
	v_lshl_add_u64 v[66:67], v[68:69], 0, s[0:1]
	v_lshl_add_u64 v[68:69], v[66:67], 0, s[0:1]
	v_lshl_add_u64 v[66:67], v[68:69], 0, s[0:1]
	v_lshl_add_u64 v[68:69], v[66:67], 0, s[0:1]
	v_lshl_add_u64 v[66:67], v[68:69], 0, s[0:1]
	v_lshl_add_u64 v[66:67], v[66:67], 0, s[0:1]
	v_lshl_add_u64 v[66:67], v[66:67], 0, s[0:1]
	v_lshl_add_u64 v[66:67], v[66:67], 0, s[0:1]
	v_lshl_add_u64 v[66:67], v[66:67], 0, s[0:1]
	v_lshl_add_u64 v[66:67], v[66:67], 0, s[0:1]
	v_lshl_add_u64 v[70:71], v[66:67], 0, s[0:1]
	v_lshl_add_u64 v[70:71], v[70:71], 0, s[0:1]
	s_waitcnt vmcnt(13)
	v_mul_f32_e32 v8, 0x44000000, v8
	v_mul_f32_e32 v4, 0x44000000, v4
	v_mov_b32_e32 v135, v49
	v_cvt_pk_fp8_f32 v135, v8, v4
	v_mul_f32_e32 v0, 0x44000000, v0
	s_waitcnt vmcnt(1)
	v_mul_f32_e32 v4, 0x44000000, v24
	v_mov_b32_e32 v136, v49
	v_cvt_pk_fp8_f32 v135, v0, v4 op_sel:[0,0,1]
	s_waitcnt vmcnt(0)
	v_mul_f32_e32 v0, 0x44000000, v63
	v_mul_f32_e32 v4, 0x44000000, v59
	v_cvt_pk_fp8_f32 v136, v0, v4
	v_mul_f32_e32 v0, 0x44000000, v45
	v_mul_f32_e32 v4, 0x44000000, v41
	v_mov_b32_e32 v137, v49
	v_cvt_pk_fp8_f32 v137, v0, v4
	v_mul_f32_e32 v28, 0x44000000, v28
	v_mul_f32_e32 v20, 0x44000000, v20
	v_mov_b32_e32 v134, v49
	v_mul_f32_e32 v0, 0x44000000, v37
	v_mul_f32_e32 v4, 0x44000000, v33
	v_mul_f32_e32 v62, 0x44000000, v62
	v_mul_f32_e32 v58, 0x44000000, v58
	v_mov_b32_e32 v132, v49
	v_mul_f32_e32 v44, 0x44000000, v44
	v_mul_f32_e32 v40, 0x44000000, v40
	v_mov_b32_e32 v133, v49
	v_cvt_pk_fp8_f32 v134, v28, v20
	v_cvt_pk_fp8_f32 v137, v0, v4 op_sel:[0,0,1]
	v_mul_f32_e32 v0, 0x44000000, v29
	v_mul_f32_e32 v4, 0x44000000, v21
	v_mov_b32_e32 v138, v49
	v_cvt_pk_fp8_f32 v132, v62, v58
	v_cvt_pk_fp8_f32 v133, v44, v40
	v_cvt_pk_fp8_f32 v138, v0, v4
	v_mul_f32_e32 v0, 0x44000000, v9
	v_mul_f32_e32 v4, 0x44000000, v5
	v_mov_b32_e32 v139, v49
	v_cvt_pk_fp8_f32 v139, v0, v4
	v_mul_f32_e32 v16, 0x44000000, v16
	v_mul_f32_e32 v12, 0x44000000, v12
	v_mul_f32_e32 v54, 0x44000000, v54
	v_mul_f32_e32 v50, 0x44000000, v50
	v_mul_f32_e32 v36, 0x44000000, v36
	v_mul_f32_e32 v32, 0x44000000, v32
	v_cvt_pk_fp8_f32 v134, v16, v12 op_sel:[0,0,1]
	v_mul_f32_e32 v8, 0x44000000, v55
	v_mul_f32_e32 v12, 0x44000000, v51
	v_cvt_pk_fp8_f32 v132, v54, v50 op_sel:[0,0,1]
	v_cvt_pk_fp8_f32 v133, v36, v32 op_sel:[0,0,1]
	v_cvt_pk_fp8_f32 v136, v8, v12 op_sel:[0,0,1]
	v_mul_f32_e32 v8, 0x44000000, v17
	v_mul_f32_e32 v12, 0x44000000, v13
	v_mul_f32_e32 v0, 0x44000000, v1
	v_mul_f32_e32 v1, 0x44000000, v25
	v_lshlrev_b32_e32 v48, 11, v48
	v_cvt_pk_fp8_f32 v138, v8, v12 op_sel:[0,0,1]
	v_cvt_pk_fp8_f32 v139, v0, v1 op_sel:[0,0,1]
	v_lshl_add_u64 v[0:1], s[8:9], 0, v[48:49]
	v_lshl_add_u64 v[0:1], v[0:1], 0, v[130:131]
	global_store_dwordx4 v[0:1], v[132:135], off sc1
	global_store_dwordx4 v[0:1], v[136:139], off offset:2048 sc1
	v_mul_f32_e32 v4, 0x44000000, v64
	v_mul_f32_e32 v5, 0x44000000, v60
	v_mov_b32_e32 v132, v49
	v_cvt_pk_fp8_f32 v132, v4, v5
	v_mul_f32_e32 v4, 0x44000000, v46
	v_mul_f32_e32 v5, 0x44000000, v42
	v_mov_b32_e32 v133, v49
	v_cvt_pk_fp8_f32 v133, v4, v5
	v_mul_f32_e32 v4, 0x44000000, v38
	v_mul_f32_e32 v5, 0x44000000, v34
	v_mov_b32_e32 v134, v49
	v_cvt_pk_fp8_f32 v133, v4, v5 op_sel:[0,0,1]
	v_mul_f32_e32 v4, 0x44000000, v30
	v_mul_f32_e32 v5, 0x44000000, v22
	v_cvt_pk_fp8_f32 v134, v4, v5
	v_mul_f32_e32 v4, 0x44000000, v10
	v_mul_f32_e32 v5, 0x44000000, v6
	v_mov_b32_e32 v135, v49
	v_cvt_pk_fp8_f32 v135, v4, v5
	v_mul_f32_e32 v8, 0x44000000, v56
	v_mul_f32_e32 v9, 0x44000000, v52
	v_mul_f32_e32 v2, 0x44000000, v2
	v_mul_f32_e32 v4, 0x44000000, v26
	v_cvt_pk_fp8_f32 v132, v8, v9 op_sel:[0,0,1]
	v_mul_f32_e32 v8, 0x44000000, v18
	v_mul_f32_e32 v9, 0x44000000, v14
	v_cvt_pk_fp8_f32 v135, v2, v4 op_sel:[0,0,1]
	v_mul_f32_e32 v2, 0x44000000, v65
	v_mul_f32_e32 v5, 0x44000000, v61
	v_mov_b32_e32 v4, v49
	v_cvt_pk_fp8_f32 v134, v8, v9 op_sel:[0,0,1]
	v_cvt_pk_fp8_f32 v4, v2, v5
	v_mul_f32_e32 v2, 0x44000000, v47
	v_mul_f32_e32 v9, 0x44000000, v43
	v_mov_b32_e32 v5, v49
	v_cvt_pk_fp8_f32 v5, v2, v9
	v_mul_f32_e32 v6, 0x44000000, v57
	v_mul_f32_e32 v8, 0x44000000, v53
	v_cvt_pk_fp8_f32 v4, v6, v8 op_sel:[0,0,1]
	v_mul_f32_e32 v2, 0x44000000, v39
	v_mul_f32_e32 v6, 0x44000000, v35
	v_cvt_pk_fp8_f32 v5, v2, v6 op_sel:[0,0,1]
	v_mul_f32_e32 v2, 0x44000000, v31
	v_mul_f32_e32 v8, 0x44000000, v23
	v_mov_b32_e32 v6, v49
	v_cvt_pk_fp8_f32 v6, v2, v8
	v_mul_f32_e32 v2, 0x44000000, v11
	v_mul_f32_e32 v8, 0x44000000, v7
	v_mov_b32_e32 v7, v49
	v_cvt_pk_fp8_f32 v7, v2, v8
	v_mul_f32_e32 v9, 0x44000000, v19
	v_mul_f32_e32 v10, 0x44000000, v15
	v_mul_f32_e32 v2, 0x44000000, v3
	v_mul_f32_e32 v3, 0x44000000, v27
	s_movk_i32 s0, 0x1000
	v_cvt_pk_fp8_f32 v6, v9, v10 op_sel:[0,0,1]
	v_cvt_pk_fp8_f32 v7, v2, v3 op_sel:[0,0,1]
	v_add_co_u32_e32 v0, vcc, s0, v0
	s_waitcnt vmcnt(16)
	v_mul_f32_e32 v2, 0x44000000, v86
	v_addc_co_u32_e32 v1, vcc, 0, v1, vcc
	global_store_dwordx4 v[0:1], v[132:135], off sc1
	global_store_dwordx4 v[0:1], v[4:7], off offset:2048 sc1
	s_branch .Lside_done_5
	v_mul_f32_e32 v1, 0x44000000, v82
	v_mov_b32_e32 v0, v49
	v_cvt_pk_fp8_f32 v0, v1, v2
	s_waitcnt vmcnt(15)
	v_mul_f32_e32 v2, 0x44000000, v110
	s_waitcnt vmcnt(14)
	v_mul_f32_e32 v5, 0x44000000, v114
	v_mov_b32_e32 v1, v49
	v_cvt_pk_fp8_f32 v1, v2, v5
	v_mul_f32_e32 v3, 0x44000000, v122
	v_mul_f32_e32 v4, 0x44000000, v126
	v_cvt_pk_fp8_f32 v0, v3, v4 op_sel:[0,0,1]
	s_waitcnt vmcnt(13)
	v_mul_f32_e32 v2, 0x44000000, v90
	s_waitcnt vmcnt(12)
	v_mul_f32_e32 v3, 0x44000000, v94
	v_cvt_pk_fp8_f32 v1, v2, v3 op_sel:[0,0,1]
	s_waitcnt vmcnt(11)
	v_mul_f32_e32 v3, 0x44000000, v74
	s_waitcnt vmcnt(10)
	v_mul_f32_e32 v4, 0x44000000, v98
	v_mov_b32_e32 v2, v49
	v_cvt_pk_fp8_f32 v2, v3, v4
	s_waitcnt vmcnt(7)
	v_mul_f32_e32 v4, 0x44000000, v78
	s_waitcnt vmcnt(6)
	v_mul_f32_e32 v7, 0x44000000, v102
	v_mov_b32_e32 v3, v49
	v_cvt_pk_fp8_f32 v3, v4, v7
	v_mul_f32_e32 v5, 0x44000000, v106
	v_mul_f32_e32 v6, 0x44000000, v118
	v_cvt_pk_fp8_f32 v2, v5, v6 op_sel:[0,0,1]
	s_waitcnt vmcnt(5)
	v_mul_f32_e32 v4, 0x44000000, v66
	s_waitcnt vmcnt(4)
	v_mul_f32_e32 v5, 0x44000000, v70
	v_cvt_pk_fp8_f32 v3, v4, v5 op_sel:[0,0,1]
	v_mul_f32_e32 v5, 0x44000000, v83
	v_mul_f32_e32 v6, 0x44000000, v87
	v_mov_b32_e32 v4, v49
	v_cvt_pk_fp8_f32 v4, v5, v6
	v_mul_f32_e32 v6, 0x44000000, v111
	v_mul_f32_e32 v9, 0x44000000, v115
	v_mov_b32_e32 v5, v49
	v_cvt_pk_fp8_f32 v5, v6, v9
	v_mul_f32_e32 v7, 0x44000000, v123
	v_mul_f32_e32 v8, 0x44000000, v127
	v_cvt_pk_fp8_f32 v4, v7, v8 op_sel:[0,0,1]
	v_mul_f32_e32 v6, 0x44000000, v91
	v_mul_f32_e32 v7, 0x44000000, v95
	v_cvt_pk_fp8_f32 v5, v6, v7 op_sel:[0,0,1]
	v_mul_f32_e32 v7, 0x44000000, v75
	v_mul_f32_e32 v8, 0x44000000, v99
	v_mov_b32_e32 v6, v49
	v_cvt_pk_fp8_f32 v6, v7, v8
	v_mul_f32_e32 v8, 0x44000000, v79
	v_mul_f32_e32 v11, 0x44000000, v103
	v_mov_b32_e32 v7, v49
	v_cvt_pk_fp8_f32 v7, v8, v11
	v_mul_f32_e32 v9, 0x44000000, v107
	v_mul_f32_e32 v10, 0x44000000, v119
	v_cvt_pk_fp8_f32 v6, v9, v10 op_sel:[0,0,1]
	v_mul_f32_e32 v8, 0x44000000, v67
	v_mul_f32_e32 v9, 0x44000000, v71
	v_cvt_pk_fp8_f32 v7, v8, v9 op_sel:[0,0,1]
	v_lshl_add_u64 v[8:9], s[4:5], 0, v[48:49]
	v_lshl_add_u64 v[8:9], v[8:9], 0, v[130:131]
	global_store_dwordx4 v[8:9], v[0:3], off sc1
	global_store_dwordx4 v[8:9], v[4:7], off offset:2048 sc1
	v_mov_b32_e32 v46, v49
	v_mul_f32_e32 v1, 0x44000000, v84
	v_mul_f32_e32 v2, 0x44000000, v88
	v_mov_b32_e32 v0, v49
	v_cvt_pk_fp8_f32 v0, v1, v2
	v_mul_f32_e32 v2, 0x44000000, v112
	v_mul_f32_e32 v5, 0x44000000, v116
	v_mov_b32_e32 v1, v49
	v_cvt_pk_fp8_f32 v1, v2, v5
	v_mul_f32_e32 v3, 0x44000000, v124
	v_mul_f32_e32 v4, 0x44000000, v128
	v_cvt_pk_fp8_f32 v0, v3, v4 op_sel:[0,0,1]
	v_mul_f32_e32 v2, 0x44000000, v92
	v_mul_f32_e32 v3, 0x44000000, v96
	v_cvt_pk_fp8_f32 v1, v2, v3 op_sel:[0,0,1]
	v_mul_f32_e32 v3, 0x44000000, v76
	v_mul_f32_e32 v4, 0x44000000, v100
	v_mov_b32_e32 v2, v49
	v_cvt_pk_fp8_f32 v2, v3, v4
	v_mul_f32_e32 v4, 0x44000000, v80
	v_mul_f32_e32 v7, 0x44000000, v104
	v_mov_b32_e32 v3, v49
	v_cvt_pk_fp8_f32 v3, v4, v7
	v_mul_f32_e32 v5, 0x44000000, v108
	v_mul_f32_e32 v6, 0x44000000, v120
	v_cvt_pk_fp8_f32 v2, v5, v6 op_sel:[0,0,1]
	v_mul_f32_e32 v4, 0x44000000, v68
	v_mul_f32_e32 v5, 0x44000000, v72
	v_cvt_pk_fp8_f32 v3, v4, v5 op_sel:[0,0,1]
	v_mul_f32_e32 v4, 0x44000000, v85
	v_mul_f32_e32 v5, 0x44000000, v89
	v_cvt_pk_fp8_f32 v46, v4, v5
	v_mul_f32_e32 v4, 0x44000000, v113
	v_mul_f32_e32 v5, 0x44000000, v117
	v_mov_b32_e32 v47, v49
	v_cvt_pk_fp8_f32 v47, v4, v5
	v_mul_f32_e32 v4, 0x44000000, v93
	v_mul_f32_e32 v5, 0x44000000, v97
	v_mov_b32_e32 v48, v49
	v_cvt_pk_fp8_f32 v47, v4, v5 op_sel:[0,0,1]
	v_mul_f32_e32 v4, 0x44000000, v77
	v_mul_f32_e32 v5, 0x44000000, v101
	v_cvt_pk_fp8_f32 v48, v4, v5
	v_mul_f32_e32 v4, 0x44000000, v81
	v_mul_f32_e32 v5, 0x44000000, v105
	v_cvt_pk_fp8_f32 v49, v4, v5
	v_mul_f32_e32 v6, 0x44000000, v125
	v_mul_f32_e32 v7, 0x44000000, v129
	v_cvt_pk_fp8_f32 v46, v6, v7 op_sel:[0,0,1]
	v_mul_f32_e32 v6, 0x44000000, v109
	v_mul_f32_e32 v7, 0x44000000, v121
	v_mul_f32_e32 v4, 0x44000000, v69
	v_mul_f32_e32 v5, 0x44000000, v73
	v_cvt_pk_fp8_f32 v48, v6, v7 op_sel:[0,0,1]
	v_cvt_pk_fp8_f32 v49, v4, v5 op_sel:[0,0,1]
	v_add_co_u32_e32 v4, vcc, s0, v8
	s_nop 1
	v_addc_co_u32_e32 v5, vcc, 0, v9, vcc
	global_store_dwordx4 v[4:5], v[0:3], off sc1
	global_store_dwordx4 v[4:5], v[46:49], off offset:2048 sc1
.Lside_done_5:
	s_waitcnt vmcnt(0)
.LBB0_922:
	s_mov_b64 s[4:5], 0

.LBB0_1054:
	s_or_b64 exec, exec, s[14:15]
	s_waitcnt lgkmcnt(0)
	s_barrier
	s_waitcnt vmcnt(5)
	ds_read_b32 v0, v135
	s_waitcnt lgkmcnt(0)
	s_barrier
	v_readfirstlane_b32 s26, v0
	s_cmpk_gt_i32 s26, 0x38ff
	s_cselect_b64 s[14:15], -1, 0
	s_and_b64 vcc, exec, s[14:15]
	s_cbranch_vccnz .LBB0_1051
	s_mov_b64 s[16:17], exec
	v_readlane_b32 s18, v255, 24
	v_readlane_b32 s19, v255, 25
	s_and_b64 s[18:19], s[16:17], s[18:19]
	s_mov_b64 exec, s[18:19]
	s_cbranch_execz .LBB0_1059
	s_mov_b64 s[20:21], exec
	v_mbcnt_lo_u32_b32 v0, s20, 0
	v_mbcnt_hi_u32_b32 v0, s21, v0
	v_cmp_eq_u32_e32 vcc, 0, v0
	s_and_saveexec_b64 s[18:19], vcc
	s_cbranch_execz .LBB0_1058
	s_bcnt1_i32_b64 s12, s[20:21]
	s_lshl_b32 s12, s12, 4
	v_mov_b32_e32 v1, s12
	global_atomic_add v1, v129, v1, s[8:9] sc0
